# phase 7 router GEMM rewritten by hand: W fragments prefetched 2 k-steps ahead (3-slot register ring, SGPR-base loads), LDS A fragments double-buffered, same accumulation order
# speedup vs baseline: 1.0363x; 1.0101x over previous
.LBB0_883:
	s_lshl_b32 s58, s57, 5
	v_or_b32_e32 v194, s58, v129
	v_ashrrev_i32_e32 v195, 31, v194
	v_lshlrev_b64 v[190:191], 11, v[194:195]
	v_or_b32_e32 v8, v190, v128
	v_mov_b32_e32 v9, v191
	v_lshlrev_b64 v[10:11], 1, v[8:9]
	v_lshl_add_u64 v[4:5], s[22:23], 0, v[10:11]
	global_load_dwordx2 v[156:157], v[4:5], off nt
	s_waitcnt lgkmcnt(0)
	v_lshl_add_u64 v[12:13], v[8:9], 2, s[26:27]
	v_or_b32_e32 v4, 0x200, v10
	v_mov_b32_e32 v5, v11
	v_lshl_add_u64 v[14:15], s[22:23], 0, v[4:5]
	global_load_dwordx4 v[4:7], v[12:13], off nt
	global_load_dwordx4 v[124:127], v[12:13], off offset:1024 nt
	v_or_b32_e32 v16, 0x400, v10
	v_mov_b32_e32 v17, v11
	v_or_b32_e32 v10, 0x600, v10
	global_load_dwordx4 v[120:123], v[12:13], off offset:2048 nt
	global_load_dwordx4 v[116:119], v[12:13], off offset:3072 nt
	v_or_b32_e32 v12, 0x400, v8
	v_mov_b32_e32 v13, v191
	v_lshl_add_u64 v[16:17], s[22:23], 0, v[16:17]
	v_lshl_add_u64 v[10:11], s[22:23], 0, v[10:11]
	v_lshl_add_u64 v[18:19], v[12:13], 1, s[22:23]
	global_load_dwordx2 v[196:197], v[14:15], off nt
	global_load_dwordx2 v[230:231], v[16:17], off nt
	global_load_dwordx2 v[218:219], v[10:11], off nt
	global_load_dwordx2 v[228:229], v[18:19], off nt
	v_lshl_add_u64 v[10:11], v[12:13], 2, s[26:27]
	global_load_dwordx4 v[112:115], v[10:11], off nt
	v_or_b32_e32 v10, 0x500, v8
	v_mov_b32_e32 v11, v191
	v_lshl_add_u64 v[12:13], v[10:11], 1, s[22:23]
	global_load_dwordx2 v[226:227], v[12:13], off nt
	v_lshl_add_u64 v[10:11], v[10:11], 2, s[26:27]
	global_load_dwordx4 v[108:111], v[10:11], off nt
	v_or_b32_e32 v10, 0x600, v8
	v_mov_b32_e32 v11, v191
	v_lshl_add_u64 v[12:13], v[10:11], 1, s[22:23]
	global_load_dwordx2 v[222:223], v[12:13], off nt
	v_lshl_add_u64 v[10:11], v[10:11], 2, s[26:27]
	v_or_b32_e32 v8, 0x700, v8
	global_load_dwordx4 v[104:107], v[10:11], off nt
	v_lshl_add_u64 v[10:11], v[8:9], 1, s[22:23]
	global_load_dwordx2 v[220:221], v[10:11], off nt
	v_lshl_add_u64 v[8:9], v[8:9], 2, s[26:27]
	v_or_b32_e32 v208, 1, v194
	global_load_dwordx4 v[100:103], v[8:9], off nt
	v_ashrrev_i32_e32 v209, 31, v208
	v_lshlrev_b64 v[192:193], 11, v[208:209]
	v_or_b32_e32 v8, v192, v128
	v_mov_b32_e32 v9, v193
	v_lshlrev_b64 v[10:11], 1, v[8:9]
	v_lshl_add_u64 v[12:13], s[22:23], 0, v[10:11]
	global_load_dwordx2 v[210:211], v[12:13], off nt
	v_lshl_add_u64 v[12:13], v[8:9], 2, s[26:27]
	global_load_dwordx4 v[96:99], v[12:13], off nt
	global_load_dwordx4 v[92:95], v[12:13], off offset:1024 nt
	v_or_b32_e32 v14, 0x200, v10
	v_mov_b32_e32 v15, v11
	v_lshl_add_u64 v[14:15], s[22:23], 0, v[14:15]
	v_or_b32_e32 v16, 0x400, v10
	v_mov_b32_e32 v17, v11
	v_or_b32_e32 v10, 0x600, v10
	global_load_dwordx4 v[88:91], v[12:13], off offset:2048 nt
	global_load_dwordx4 v[84:87], v[12:13], off offset:3072 nt
	v_or_b32_e32 v12, 0x400, v8
	v_mov_b32_e32 v13, v193
	v_lshl_add_u64 v[16:17], s[22:23], 0, v[16:17]
	v_lshl_add_u64 v[10:11], s[22:23], 0, v[10:11]
	v_lshl_add_u64 v[18:19], v[12:13], 1, s[22:23]
	global_load_dwordx2 v[224:225], v[14:15], off nt
	global_load_dwordx2 v[202:203], v[16:17], off nt
	global_load_dwordx2 v[216:217], v[10:11], off nt
	global_load_dwordx2 v[214:215], v[18:19], off nt
	v_lshl_add_u64 v[10:11], v[12:13], 2, s[26:27]
	global_load_dwordx4 v[80:83], v[10:11], off nt
	v_or_b32_e32 v10, 0x500, v8
	v_mov_b32_e32 v11, v193
	v_lshl_add_u64 v[12:13], v[10:11], 1, s[22:23]
	global_load_dwordx2 v[212:213], v[12:13], off nt
	v_lshl_add_u64 v[10:11], v[10:11], 2, s[26:27]
	global_load_dwordx4 v[76:79], v[10:11], off nt
	v_or_b32_e32 v10, 0x600, v8
	v_mov_b32_e32 v11, v193
	v_lshl_add_u64 v[12:13], v[10:11], 1, s[22:23]
	global_load_dwordx2 v[206:207], v[12:13], off nt
	v_lshl_add_u64 v[10:11], v[10:11], 2, s[26:27]
	v_or_b32_e32 v8, 0x700, v8
	v_or_b32_e32 v184, 2, v194
	global_load_dwordx4 v[72:75], v[10:11], off nt
	v_lshl_add_u64 v[10:11], v[8:9], 1, s[22:23]
	v_ashrrev_i32_e32 v185, 31, v184
	global_load_dwordx2 v[204:205], v[10:11], off nt
	v_lshl_add_u64 v[8:9], v[8:9], 2, s[26:27]
	v_lshlrev_b64 v[150:151], 11, v[184:185]
	global_load_dwordx4 v[68:71], v[8:9], off nt
	v_or_b32_e32 v8, v150, v128
	v_mov_b32_e32 v9, v151
	v_lshlrev_b64 v[10:11], 1, v[8:9]
	v_lshl_add_u64 v[12:13], s[22:23], 0, v[10:11]
	global_load_dwordx2 v[186:187], v[12:13], off nt
	v_lshl_add_u64 v[12:13], v[8:9], 2, s[26:27]
	v_or_b32_e32 v14, 0x200, v10
	v_mov_b32_e32 v15, v11
	v_or_b32_e32 v16, 0x400, v10
	v_or_b32_e32 v10, 0x600, v10
	v_lshl_add_u64 v[14:15], s[22:23], 0, v[14:15]
	global_load_dwordx4 v[64:67], v[12:13], off nt
	global_load_dwordx4 v[60:63], v[12:13], off offset:1024 nt
	v_mov_b32_e32 v17, v11
	v_lshl_add_u64 v[10:11], s[22:23], 0, v[10:11]
	global_load_dwordx4 v[56:59], v[12:13], off offset:2048 nt
	global_load_dwordx4 v[52:55], v[12:13], off offset:3072 nt
	v_or_b32_e32 v12, 0x400, v8
	v_mov_b32_e32 v13, v151
	v_lshl_add_u64 v[16:17], s[22:23], 0, v[16:17]
	v_lshl_add_u64 v[18:19], v[12:13], 1, s[22:23]
	global_load_dwordx2 v[188:189], v[14:15], off nt
	global_load_dwordx2 v[182:183], v[16:17], off nt
	global_load_dwordx2 v[180:181], v[10:11], off nt
	global_load_dwordx2 v[178:179], v[18:19], off nt
	v_lshl_add_u64 v[10:11], v[12:13], 2, s[26:27]
	global_load_dwordx4 v[48:51], v[10:11], off nt
	v_or_b32_e32 v10, 0x500, v8
	v_mov_b32_e32 v11, v151
	v_lshl_add_u64 v[12:13], v[10:11], 1, s[22:23]
	v_lshl_add_u64 v[10:11], v[10:11], 2, s[26:27]
	v_or_b32_e32 v166, 3, v194
	global_load_dwordx4 v[44:47], v[10:11], off nt
	v_or_b32_e32 v10, 0x600, v8
	v_mov_b32_e32 v11, v151
	v_ashrrev_i32_e32 v167, 31, v166
	global_load_dwordx2 v[176:177], v[12:13], off nt
	v_lshl_add_u64 v[12:13], v[10:11], 1, s[22:23]
	v_lshl_add_u64 v[10:11], v[10:11], 2, s[26:27]
	v_or_b32_e32 v8, 0x700, v8
	v_lshlrev_b64 v[252:253], 11, v[166:167]
	global_load_dwordx4 v[40:43], v[10:11], off nt
	v_lshl_add_u64 v[10:11], v[8:9], 1, s[22:23]
	v_lshl_add_u64 v[8:9], v[8:9], 2, s[26:27]
	v_or_b32_e32 v198, v252, v128
	v_mov_b32_e32 v199, v253
	global_load_dwordx4 v[36:39], v[8:9], off nt
	v_lshlrev_b64 v[8:9], 1, v[198:199]
	global_load_dwordx2 v[174:175], v[12:13], off nt
	global_load_dwordx2 v[172:173], v[10:11], off nt
	v_lshl_add_u64 v[10:11], s[22:23], 0, v[8:9]
	global_load_dwordx2 v[168:169], v[10:11], off nt
	v_lshl_add_u64 v[10:11], v[198:199], 2, s[26:27]
	v_or_b32_e32 v12, 0x200, v8
	v_mov_b32_e32 v13, v9
	v_or_b32_e32 v14, 0x400, v8
	v_or_b32_e32 v8, 0x600, v8
	v_lshl_add_u64 v[12:13], s[22:23], 0, v[12:13]
	global_load_dwordx4 v[32:35], v[10:11], off nt
	global_load_dwordx4 v[28:31], v[10:11], off offset:1024 nt
	v_mov_b32_e32 v15, v9
	v_lshl_add_u64 v[8:9], s[22:23], 0, v[8:9]
	global_load_dwordx4 v[24:27], v[10:11], off offset:2048 nt
	global_load_dwordx4 v[20:23], v[10:11], off offset:3072 nt
	v_or_b32_e32 v10, 0x400, v198
	v_mov_b32_e32 v11, v253
	v_lshl_add_u64 v[14:15], s[22:23], 0, v[14:15]
	v_lshl_add_u64 v[16:17], v[10:11], 1, s[22:23]
	global_load_dwordx2 v[170:171], v[12:13], off nt
	global_load_dwordx2 v[164:165], v[14:15], off nt
	global_load_dwordx2 v[162:163], v[8:9], off nt
	global_load_dwordx2 v[160:161], v[16:17], off nt
	v_lshl_add_u64 v[8:9], v[10:11], 2, s[26:27]
	global_load_dwordx4 v[16:19], v[8:9], off nt
	v_or_b32_e32 v8, 0x500, v198
	v_mov_b32_e32 v9, v253
	s_waitcnt vmcnt(57)
	v_lshlrev_b32_e32 v200, 16, v156
	v_and_b32_e32 v201, 0xffff0000, v156
	v_or_b32_e32 v152, 0x700, v198
	v_mov_b32_e32 v153, v253
	v_lshl_add_u64 v[10:11], v[8:9], 1, s[22:23]
	v_lshl_add_u64 v[8:9], v[8:9], 2, s[26:27]
	v_lshlrev_b32_e32 v156, 16, v157
	v_and_b32_e32 v157, 0xffff0000, v157
	s_waitcnt vmcnt(56)
	v_pk_add_f32 v[200:201], v[4:5], v[200:201]
	v_lshl_add_u64 v[4:5], v[152:153], 1, s[22:23]
	global_load_dwordx4 v[12:15], v[8:9], off nt
	v_or_b32_e32 v8, 0x600, v198
	v_mov_b32_e32 v9, v253
	v_pk_add_f32 v[198:199], v[6:7], v[156:157]
	global_load_dwordx2 v[156:157], v[4:5], off nt
	v_lshl_add_u64 v[4:5], v[152:153], 2, s[26:27]
	v_lshlrev_b64 v[152:153], 12, v[194:195]
	global_load_dwordx2 v[158:159], v[10:11], off nt
	v_lshl_add_u64 v[10:11], v[8:9], 1, s[22:23]
	v_lshl_add_u64 v[8:9], v[8:9], 2, s[26:27]
	v_lshl_add_u64 v[142:143], v[130:131], 0, v[152:153]
	global_load_dwordx2 v[154:155], v[10:11], off nt
	s_bfe_i32 s10, s57, 0x150006
	global_load_dwordx4 v[8:11], v[8:9], off nt
	v_mov_b32_e32 v3, 0x3000
	global_load_dwordx4 v[4:7], v[4:5], off nt
	v_cvt_pk_bf16_f32 v194, v200, v201
	v_cvt_pk_bf16_f32 v195, v198, v199
	global_store_dwordx2 v[142:143], v[194:195], off
	s_waitcnt vmcnt(59)
	v_lshlrev_b32_e32 v142, 16, v196
	v_and_b32_e32 v143, 0xffff0000, v196
	v_lshlrev_b32_e32 v194, 16, v197
	v_and_b32_e32 v195, 0xffff0000, v197
	v_pk_add_f32 v[196:197], v[124:125], v[142:143]
	v_lshl_add_u64 v[124:125], s[76:77], 0, v[152:153]
	v_lshl_add_u64 v[124:125], v[124:125], 0, v[138:139]
	v_add_co_u32_e32 v142, vcc, s52, v124
	v_pk_add_f32 v[194:195], v[126:127], v[194:195]
	s_nop 0
	v_addc_co_u32_e32 v143, vcc, 0, v125, vcc
	v_cvt_pk_bf16_f32 v124, v196, v197
	v_cvt_pk_bf16_f32 v125, v194, v195
	global_store_dwordx2 v[142:143], v[124:125], off offset:512
	s_waitcnt vmcnt(59)
	v_lshlrev_b32_e32 v126, 16, v230
	v_and_b32_e32 v127, 0xffff0000, v230
	v_lshlrev_b32_e32 v124, 16, v231
	v_and_b32_e32 v125, 0xffff0000, v231
	v_mul_i32_i24_e32 v152, s10, v3
	v_pk_add_f32 v[124:125], v[122:123], v[124:125]
	v_pk_add_f32 v[126:127], v[120:121], v[126:127]
	v_ashrrev_i32_e32 v153, 31, v152
	v_cvt_pk_bf16_f32 v120, v126, v127
	v_cvt_pk_bf16_f32 v121, v124, v125
	global_store_dwordx2 v[142:143], v[120:121], off offset:1024
	s_waitcnt vmcnt(59)
	v_lshlrev_b32_e32 v120, 16, v219
	v_and_b32_e32 v121, 0xffff0000, v219
	v_lshlrev_b64 v[152:153], 2, v[152:153]
	v_lshlrev_b32_e32 v122, 16, v218
	v_and_b32_e32 v123, 0xffff0000, v218
	v_lshl_add_u64 v[218:219], s[16:17], 0, v[152:153]
	v_pk_add_f32 v[120:121], v[118:119], v[120:121]
	s_waitcnt vmcnt(58)
	v_lshlrev_b32_e32 v118, 16, v228
	v_and_b32_e32 v119, 0xffff0000, v228
	v_lshlrev_b32_e32 v152, 16, v229
	v_and_b32_e32 v153, 0xffff0000, v229
	v_pk_add_f32 v[122:123], v[116:117], v[122:123]
	s_waitcnt vmcnt(57)
	v_pk_add_f32 v[114:115], v[114:115], v[152:153]
	v_cvt_pk_bf16_f32 v116, v122, v123
	v_cvt_pk_bf16_f32 v117, v120, v121
	global_store_dwordx2 v[142:143], v[116:117], off offset:1536
	v_pk_add_f32 v[112:113], v[112:113], v[118:119]
	s_waitcnt vmcnt(57)
	v_lshlrev_b32_e32 v152, 16, v227
	v_cvt_pk_bf16_f32 v118, v112, v113
	v_cvt_pk_bf16_f32 v119, v114, v115
	global_store_dwordx2 v[142:143], v[118:119], off offset:2048
	v_lshlrev_b32_e32 v118, 16, v226
	v_and_b32_e32 v119, 0xffff0000, v226
	v_and_b32_e32 v153, 0xffff0000, v227
	s_waitcnt vmcnt(57)
	v_pk_add_f32 v[108:109], v[108:109], v[118:119]
	v_pk_add_f32 v[110:111], v[110:111], v[152:153]
	v_cvt_pk_bf16_f32 v118, v108, v109
	v_mov_b32_e32 v152, v113
	v_cvt_pk_bf16_f32 v119, v110, v111
	v_mov_b32_e32 v153, v109
	global_store_dwordx2 v[142:143], v[118:119], off offset:2560
	v_mov_b32_e32 v118, v112
	v_mov_b32_e32 v119, v108
	v_pk_mul_f32 v[152:153], v[152:153], v[152:153]
	v_xor_b32_e32 v3, 32, v246
	v_pk_fma_f32 v[118:119], v[118:119], v[118:119], v[152:153]
	v_mov_b32_e32 v152, v114
	v_mov_b32_e32 v153, v110
	v_pk_fma_f32 v[118:119], v[152:153], v[152:153], v[118:119]
	v_mov_b32_e32 v152, v115
	v_mov_b32_e32 v153, v111
	v_pk_fma_f32 v[226:227], v[152:153], v[152:153], v[118:119]
	s_waitcnt vmcnt(57)
	v_lshlrev_b32_e32 v118, 16, v222
	v_and_b32_e32 v119, 0xffff0000, v222
	v_lshlrev_b32_e32 v152, 16, v223
	v_and_b32_e32 v153, 0xffff0000, v223
	s_waitcnt vmcnt(56)
	v_pk_add_f32 v[106:107], v[106:107], v[152:153]
	v_pk_add_f32 v[104:105], v[104:105], v[118:119]
	s_waitcnt vmcnt(55)
	v_lshlrev_b32_e32 v152, 16, v221
	v_cvt_pk_bf16_f32 v118, v104, v105
	v_cvt_pk_bf16_f32 v119, v106, v107
	global_store_dwordx2 v[142:143], v[118:119], off offset:3072
	v_lshlrev_b32_e32 v118, 16, v220
	v_and_b32_e32 v119, 0xffff0000, v220
	v_and_b32_e32 v153, 0xffff0000, v221
	s_waitcnt vmcnt(55)
	v_pk_add_f32 v[100:101], v[100:101], v[118:119]
	v_pk_add_f32 v[102:103], v[102:103], v[152:153]
	v_cvt_pk_bf16_f32 v118, v100, v101
	s_waitcnt vmcnt(54)
	v_lshlrev_b32_e32 v152, 16, v211
	v_cvt_pk_bf16_f32 v119, v102, v103
	global_store_dwordx2 v[142:143], v[118:119], off offset:3584
	v_mov_b32_e32 v142, v105
	v_mov_b32_e32 v143, v101
	v_mov_b32_e32 v118, v104
	v_mov_b32_e32 v119, v100
	v_pk_mul_f32 v[142:143], v[142:143], v[142:143]
	v_and_b32_e32 v153, 0xffff0000, v211
	v_pk_fma_f32 v[118:119], v[118:119], v[118:119], v[142:143]
	v_mov_b32_e32 v142, v106
	v_mov_b32_e32 v143, v102
	v_pk_fma_f32 v[118:119], v[142:143], v[142:143], v[118:119]
	v_mov_b32_e32 v142, v107
	v_mov_b32_e32 v143, v103
	v_pk_fma_f32 v[228:229], v[142:143], v[142:143], v[118:119]
	v_lshlrev_b64 v[118:119], 12, v[208:209]
	v_lshlrev_b32_e32 v142, 16, v210
	v_and_b32_e32 v143, 0xffff0000, v210
	s_waitcnt vmcnt(54)
	v_pk_add_f32 v[220:221], v[98:99], v[152:153]
	v_lshl_add_u64 v[98:99], v[130:131], 0, v[118:119]
	v_pk_add_f32 v[222:223], v[96:97], v[142:143]
	v_cmp_lt_i32_e32 vcc, v3, v247
	v_cvt_pk_bf16_f32 v96, v222, v223
	v_cvt_pk_bf16_f32 v97, v220, v221
	global_store_dwordx2 v[98:99], v[96:97], off
	s_waitcnt vmcnt(51)
	v_lshlrev_b32_e32 v98, 16, v225
	v_and_b32_e32 v99, 0xffff0000, v225
	v_pk_add_f32 v[208:209], v[94:95], v[98:99]
	v_lshl_add_u64 v[94:95], s[76:77], 0, v[118:119]
	v_lshl_add_u64 v[94:95], v[94:95], 0, v[138:139]
	v_cndmask_b32_e32 v3, v246, v3, vcc
	v_lshlrev_b32_e32 v96, 16, v224
	v_and_b32_e32 v97, 0xffff0000, v224
	v_add_co_u32_e32 v142, vcc, s52, v94
	v_pk_add_f32 v[210:211], v[92:93], v[96:97]
	s_nop 0
	v_addc_co_u32_e32 v143, vcc, 0, v95, vcc
	v_cvt_pk_bf16_f32 v92, v210, v211
	v_cvt_pk_bf16_f32 v93, v208, v209
	global_store_dwordx2 v[142:143], v[92:93], off offset:512
	s_waitcnt vmcnt(51)
	v_lshlrev_b32_e32 v92, 16, v202
	v_and_b32_e32 v93, 0xffff0000, v202
	v_lshlrev_b32_e32 v94, 16, v203
	v_and_b32_e32 v95, 0xffff0000, v203
	v_pk_add_f32 v[98:99], v[90:91], v[94:95]
	v_pk_add_f32 v[202:203], v[88:89], v[92:93]
	s_waitcnt vmcnt(50)
	v_lshlrev_b32_e32 v90, 16, v217
	v_cvt_pk_bf16_f32 v88, v202, v203
	v_cvt_pk_bf16_f32 v89, v98, v99
	global_store_dwordx2 v[142:143], v[88:89], off offset:1024
	v_lshlrev_b32_e32 v88, 16, v216
	v_and_b32_e32 v89, 0xffff0000, v216
	v_and_b32_e32 v91, 0xffff0000, v217
	v_pk_add_f32 v[90:91], v[86:87], v[90:91]
	v_pk_add_f32 v[94:95], v[84:85], v[88:89]
	s_waitcnt vmcnt(50)
	v_lshlrev_b32_e32 v86, 16, v215
	v_cvt_pk_bf16_f32 v84, v94, v95
	v_cvt_pk_bf16_f32 v85, v90, v91
	global_store_dwordx2 v[142:143], v[84:85], off offset:1536
	v_lshlrev_b32_e32 v84, 16, v214
	v_and_b32_e32 v85, 0xffff0000, v214
	v_and_b32_e32 v87, 0xffff0000, v215
	s_waitcnt vmcnt(50)
	v_pk_add_f32 v[82:83], v[82:83], v[86:87]
	v_pk_add_f32 v[86:87], v[80:81], v[84:85]
	s_waitcnt vmcnt(49)
	v_lshlrev_b32_e32 v84, 16, v212
	v_cvt_pk_bf16_f32 v80, v86, v87
	v_cvt_pk_bf16_f32 v81, v82, v83
	v_and_b32_e32 v85, 0xffff0000, v212
	global_store_dwordx2 v[142:143], v[80:81], off offset:2048
	v_lshlrev_b32_e32 v80, 16, v213
	v_and_b32_e32 v81, 0xffff0000, v213
	s_waitcnt vmcnt(49)
	v_pk_add_f32 v[84:85], v[76:77], v[84:85]
	v_pk_add_f32 v[80:81], v[78:79], v[80:81]
	v_cvt_pk_bf16_f32 v76, v84, v85
	v_mov_b32_e32 v78, v87
	v_cvt_pk_bf16_f32 v77, v80, v81
	v_mov_b32_e32 v79, v85
	global_store_dwordx2 v[142:143], v[76:77], off offset:2560
	v_mov_b32_e32 v76, v86
	v_mov_b32_e32 v77, v84
	v_pk_mul_f32 v[78:79], v[78:79], v[78:79]
	v_mov_b32_e32 v88, v223
	v_pk_fma_f32 v[76:77], v[76:77], v[76:77], v[78:79]
	v_mov_b32_e32 v78, v82
	v_mov_b32_e32 v79, v80
	v_pk_fma_f32 v[76:77], v[78:79], v[78:79], v[76:77]
	v_mov_b32_e32 v78, v83
	v_mov_b32_e32 v79, v81
	v_mov_b32_e32 v89, v201
	v_pk_fma_f32 v[78:79], v[78:79], v[78:79], v[76:77]
	v_mov_b32_e32 v76, v222
	v_mov_b32_e32 v77, v200
	v_pk_mul_f32 v[88:89], v[88:89], v[88:89]
	v_mov_b32_e32 v92, v211
	v_pk_fma_f32 v[76:77], v[76:77], v[76:77], v[88:89]
	v_mov_b32_e32 v88, v220
	v_mov_b32_e32 v89, v198
	v_pk_fma_f32 v[76:77], v[88:89], v[88:89], v[76:77]
	v_mov_b32_e32 v88, v221
	v_mov_b32_e32 v89, v199
	v_mov_b32_e32 v93, v197
	v_pk_fma_f32 v[76:77], v[88:89], v[88:89], v[76:77]
	v_mov_b32_e32 v88, v210
	v_mov_b32_e32 v89, v196
	v_pk_mul_f32 v[92:93], v[92:93], v[92:93]
	v_lshl_add_u64 v[116:117], v[218:219], 0, s[36:37]
	v_pk_fma_f32 v[88:89], v[88:89], v[88:89], v[92:93]
	v_mov_b32_e32 v92, v208
	v_mov_b32_e32 v93, v194
	v_pk_fma_f32 v[88:89], v[92:93], v[92:93], v[88:89]
	v_mov_b32_e32 v92, v209
	v_mov_b32_e32 v93, v195
	v_pk_fma_f32 v[88:89], v[92:93], v[92:93], v[88:89]
	v_mov_b32_e32 v92, v203
	v_mov_b32_e32 v93, v127
	v_pk_add_f32 v[76:77], v[76:77], v[88:89]
	v_mov_b32_e32 v88, v202
	v_mov_b32_e32 v89, v126
	v_pk_mul_f32 v[92:93], v[92:93], v[92:93]
	v_mov_b32_e32 v212, v78
	v_pk_fma_f32 v[88:89], v[88:89], v[88:89], v[92:93]
	v_mov_b32_e32 v92, v98
	v_mov_b32_e32 v93, v124
	v_pk_fma_f32 v[88:89], v[92:93], v[92:93], v[88:89]
	v_mov_b32_e32 v92, v99
	v_mov_b32_e32 v93, v125
	v_pk_fma_f32 v[88:89], v[92:93], v[92:93], v[88:89]
	v_mov_b32_e32 v92, v95
	v_mov_b32_e32 v93, v123
	v_pk_add_f32 v[76:77], v[76:77], v[88:89]
	v_mov_b32_e32 v88, v94
	v_mov_b32_e32 v89, v122
	v_pk_mul_f32 v[92:93], v[92:93], v[92:93]
	v_mov_b32_e32 v213, v226
	v_pk_fma_f32 v[88:89], v[88:89], v[88:89], v[92:93]
	v_mov_b32_e32 v92, v90
	v_mov_b32_e32 v93, v120
	v_pk_fma_f32 v[88:89], v[92:93], v[92:93], v[88:89]
	v_mov_b32_e32 v92, v91
	v_mov_b32_e32 v93, v121
	v_pk_fma_f32 v[88:89], v[92:93], v[92:93], v[88:89]
	v_mov_b32_e32 v226, v79
	v_pk_add_f32 v[152:153], v[76:77], v[88:89]
	s_waitcnt vmcnt(49)
	v_lshlrev_b32_e32 v76, 16, v206
	v_and_b32_e32 v77, 0xffff0000, v206
	v_lshlrev_b32_e32 v88, 16, v207
	v_and_b32_e32 v89, 0xffff0000, v207
	s_waitcnt vmcnt(48)
	v_pk_add_f32 v[88:89], v[74:75], v[88:89]
	v_pk_add_f32 v[92:93], v[72:73], v[76:77]
	s_waitcnt vmcnt(47)
	v_lshlrev_b32_e32 v74, 16, v205
	v_cvt_pk_bf16_f32 v72, v92, v93
	v_cvt_pk_bf16_f32 v73, v88, v89
	global_store_dwordx2 v[142:143], v[72:73], off offset:3072
	v_lshlrev_b32_e32 v72, 16, v204
	v_and_b32_e32 v73, 0xffff0000, v204
	v_and_b32_e32 v75, 0xffff0000, v205
	s_waitcnt vmcnt(47)
	v_pk_add_f32 v[96:97], v[70:71], v[74:75]
	v_pk_add_f32 v[118:119], v[68:69], v[72:73]
	v_mov_b32_e32 v206, v93
	v_cvt_pk_bf16_f32 v68, v118, v119
	v_cvt_pk_bf16_f32 v69, v96, v97
	global_store_dwordx2 v[142:143], v[68:69], off offset:3584
	v_mov_b32_e32 v142, v128
	v_lshl_add_u64 v[68:69], v[218:219], 0, s[14:15]
	v_ashrrev_i32_e32 v143, 31, v142
	v_lshlrev_b64 v[74:75], 2, v[142:143]
	v_lshl_add_u64 v[70:71], s[28:29], 0, v[74:75]
	v_lshl_add_u64 v[76:77], v[68:69], 0, v[74:75]
	global_load_dwordx4 v[70:73], v[70:71], off
	v_lshl_add_u64 v[204:205], v[116:117], 0, v[74:75]
	global_load_dwordx4 v[74:77], v[76:77], off
	s_nop 0
	global_load_dwordx4 v[216:219], v[204:205], off
	v_mov_b32_e32 v207, v119
	v_mov_b32_e32 v204, v92
	v_mov_b32_e32 v205, v118
	v_pk_mul_f32 v[206:207], v[206:207], v[206:207]
	v_pk_add_f32 v[152:153], v[152:153], v[212:213]
	v_pk_fma_f32 v[204:205], v[204:205], v[204:205], v[206:207]
	v_mov_b32_e32 v206, v88
	v_mov_b32_e32 v207, v96
	v_pk_fma_f32 v[204:205], v[206:207], v[206:207], v[204:205]
	v_mov_b32_e32 v206, v89
	v_mov_b32_e32 v207, v97
	v_pk_fma_f32 v[204:205], v[206:207], v[206:207], v[204:205]
	v_pk_add_f32 v[78:79], v[152:153], v[226:227]
	v_mov_b32_e32 v152, v204
	v_mov_b32_e32 v153, v228
	v_pk_add_f32 v[78:79], v[78:79], v[152:153]
	v_mov_b32_e32 v228, v205
	v_lshlrev_b32_e32 v3, 2, v3
	v_pk_add_f32 v[78:79], v[78:79], v[228:229]
	ds_bpermute_b32 v153, v3, v79
	ds_bpermute_b32 v152, v3, v78
	v_xor_b32_e32 v204, 16, v246
	v_cmp_lt_i32_e32 vcc, v204, v247
	v_xor_b32_e32 v205, 8, v246
	v_lshl_add_u64 v[190:191], s[24:25], 0, v[190:191]
	v_cndmask_b32_e32 v204, v246, v204, vcc
	v_lshlrev_b32_e32 v204, 2, v204
	s_waitcnt lgkmcnt(0)
	v_pk_add_f32 v[78:79], v[78:79], v[152:153]
	ds_bpermute_b32 v153, v204, v79
	ds_bpermute_b32 v152, v204, v78
	v_cmp_lt_i32_e32 vcc, v205, v247
	v_lshl_add_u64 v[192:193], s[24:25], 0, v[192:193]
	s_waitcnt lgkmcnt(0)
	v_pk_add_f32 v[78:79], v[78:79], v[152:153]
	v_cndmask_b32_e32 v205, v246, v205, vcc
	v_lshlrev_b32_e32 v205, 2, v205
	ds_bpermute_b32 v153, v205, v79
	ds_bpermute_b32 v152, v205, v78
	v_cmp_lt_i32_e32 vcc, v0, v247
	s_waitcnt lgkmcnt(0)
	v_pk_add_f32 v[78:79], v[78:79], v[152:153]
	v_cndmask_b32_e32 v206, v246, v0, vcc
	v_lshlrev_b32_e32 v206, 2, v206
	ds_bpermute_b32 v153, v206, v79
	ds_bpermute_b32 v152, v206, v78
	v_cmp_lt_i32_e32 vcc, v249, v247
	s_waitcnt lgkmcnt(0)
	v_pk_add_f32 v[78:79], v[78:79], v[152:153]
	v_cndmask_b32_e32 v207, v246, v249, vcc
	v_lshlrev_b32_e32 v207, 2, v207
	ds_bpermute_b32 v153, v207, v79
	ds_bpermute_b32 v152, v207, v78
	v_cmp_lt_i32_e32 vcc, v254, v247
	s_waitcnt lgkmcnt(0)
	v_pk_add_f32 v[78:79], v[78:79], v[152:153]
	v_cndmask_b32_e32 v212, v246, v254, vcc
	v_lshlrev_b32_e32 v212, 2, v212
	ds_bpermute_b32 v153, v212, v79
	ds_bpermute_b32 v152, v212, v78
	s_waitcnt lgkmcnt(0)
	v_pk_add_f32 v[78:79], v[78:79], v[152:153]
	s_nop 0
	v_pk_fma_f32 v[78:79], v[78:79], s[38:39], v[140:141] op_sel_hi:[1,0,0]
	s_nop 0
	v_mul_f32_e32 v152, 0x4b800000, v79
	v_cmp_gt_f32_e32 vcc, s53, v79
	v_cmp_gt_f32_e64 s[10:11], s53, v78
	s_nop 0
	v_cndmask_b32_e32 v79, v79, v152, vcc
	v_mul_f32_e32 v152, 0x4b800000, v78
	v_rsq_f32_e32 v79, v79
	v_cndmask_b32_e64 v78, v78, v152, s[10:11]
	v_rsq_f32_e32 v78, v78
	v_mul_f32_e32 v152, 0x45800000, v79
	v_cndmask_b32_e32 v214, v79, v152, vcc
	v_mul_f32_e32 v79, 0x45800000, v78
	v_cndmask_b32_e64 v213, v78, v79, s[10:11]
	s_waitcnt vmcnt(1)
	v_add_f32_e32 v79, 1.0, v74
	v_mul_f32_e32 v74, v201, v214
	v_mul_f32_e32 v74, v74, v71
	v_add_f32_e32 v152, 1.0, v75
	s_waitcnt vmcnt(0)
	v_fma_f32 v153, v74, v152, v217
	v_mul_f32_e32 v74, v198, v214
	v_mul_f32_e32 v74, v74, v72
	v_add_f32_e32 v198, 1.0, v76
	v_mul_f32_e32 v78, v200, v214
	v_fma_f32 v200, v74, v198, v218
	v_mul_f32_e32 v74, v199, v214
	v_mul_f32_e32 v78, v78, v70
	v_mul_f32_e32 v74, v74, v73
	v_add_f32_e32 v199, 1.0, v77
	v_fma_f32 v78, v78, v79, v216
	v_fma_f32 v201, v74, v199, v219
	v_cvt_pk_bf16_f32 v74, v78, v153
	v_cvt_pk_bf16_f32 v75, v200, v201
	v_mul_f32_e32 v126, v126, v214
	v_lshlrev_b32_e32 v76, 16, v74
	v_and_b32_e32 v77, 0xffff0000, v74
	v_and_b32_e32 v224, 0xffff0000, v75
	v_sub_f32_e32 v76, v78, v76
	v_sub_f32_e32 v77, v153, v77
	v_lshlrev_b32_e32 v215, 16, v75
	v_sub_f32_e32 v224, v201, v224
	v_sub_f32_e32 v215, v200, v215
	v_cvt_pk_bf16_f32 v76, v76, v77
	v_cvt_pk_bf16_f32 v77, v215, v224
	v_mov_b32_e32 v224, 0
	v_cvt_pk_fp8_f32 v224, v78, v153
	v_mov_b32_e32 v215, v232
	v_mul_f32_e32 v84, v84, v213
	v_xor_b32_e32 v215, v215, v129
	v_lshl_add_u32 v215, v215, 4, v240
	v_cvt_pk_fp8_f32 v224, v200, v201 op_sel:[0,0,1]
	v_add_u32_e32 v78, 0, v215
	ds_write_b64 v78, v[74:75]
	v_add_u32_e32 v74, s56, v215
	ds_write_b64 v74, v[76:77]
	v_lshl_add_u64 v[74:75], v[190:191], 0, v[142:143]
	global_store_dword v[74:75], v224, off
	v_mul_f32_e32 v74, v222, v213
	v_mul_f32_e32 v70, v70, v74
	v_fma_f32 v74, v79, v70, v216
	v_mul_f32_e32 v70, v223, v213
	v_mul_f32_e32 v70, v71, v70
	v_fma_f32 v75, v152, v70, v217
	v_mul_f32_e32 v70, v220, v213
	v_mul_f32_e32 v70, v72, v70
	v_fma_f32 v76, v198, v70, v218
	v_mul_f32_e32 v70, v221, v213
	v_mul_f32_e32 v70, v73, v70
	v_fmac_f32_e32 v219, v199, v70
	v_cvt_pk_bf16_f32 v70, v74, v75
	v_cvt_pk_bf16_f32 v71, v76, v219
	v_mul_f32_e32 v85, v85, v213
	v_lshlrev_b32_e32 v72, 16, v70
	v_and_b32_e32 v73, 0xffff0000, v70
	v_and_b32_e32 v78, 0xffff0000, v71
	v_sub_f32_e32 v72, v74, v72
	v_sub_f32_e32 v73, v75, v73
	v_lshlrev_b32_e32 v77, 16, v71
	v_sub_f32_e32 v78, v219, v78
	v_sub_f32_e32 v77, v76, v77
	v_cvt_pk_bf16_f32 v72, v72, v73
	v_cvt_pk_bf16_f32 v73, v77, v78
	v_mov_b32_e32 v78, 0
	v_cvt_pk_fp8_f32 v78, v74, v75
	v_mov_b32_e32 v77, v232
	v_mul_f32_e32 v80, v80, v213
	v_xor_b32_e32 v77, v77, v235
	v_lshl_add_u32 v77, v77, 4, v241
	v_cvt_pk_fp8_f32 v78, v76, v219 op_sel:[0,0,1]
	v_add_u32_e32 v74, 0, v77
	ds_write_b64 v74, v[70:71]
	v_add_u32_e32 v70, s56, v77
	ds_write_b64 v70, v[72:73]
	v_lshl_add_u64 v[70:71], v[192:193], 0, v[142:143]
	global_store_dword v[70:71], v78, off
	v_mov_b32_e32 v78, v128
	v_mul_f32_e32 v92, v92, v213
	v_ashrrev_i32_e32 v79, 31, v78
	v_lshlrev_b64 v[70:71], 2, v[78:79]
	v_lshl_add_u64 v[74:75], v[70:71], 0, s[40:41]
	v_lshl_add_u64 v[70:71], s[28:29], 0, v[70:71]
	v_lshl_add_u64 v[76:77], v[68:69], 0, v[74:75]
	global_load_dwordx4 v[70:73], v[70:71], off offset:1024
	v_lshl_add_u64 v[142:143], v[116:117], 0, v[74:75]
	global_load_dwordx4 v[74:77], v[76:77], off
	s_nop 0
	global_load_dwordx4 v[198:201], v[142:143], off
	v_mul_f32_e32 v142, v196, v214
	v_mul_f32_e32 v93, v93, v213
	v_mul_f32_e32 v88, v88, v213
	v_mul_f32_e32 v96, v96, v213
	s_waitcnt vmcnt(2)
	v_mul_f32_e32 v142, v142, v70
	s_waitcnt vmcnt(1)
	v_add_f32_e32 v143, 1.0, v74
	v_mul_f32_e32 v74, v197, v214
	v_mul_f32_e32 v74, v74, v71
	v_add_f32_e32 v152, 1.0, v75
	s_waitcnt vmcnt(0)
	v_fma_f32 v153, v74, v152, v199
	v_mul_f32_e32 v74, v194, v214
	v_mul_f32_e32 v74, v74, v72
	v_add_f32_e32 v194, 1.0, v76
	v_fma_f32 v196, v74, v194, v200
	v_mul_f32_e32 v74, v195, v214
	v_mul_f32_e32 v74, v74, v73
	v_add_f32_e32 v195, 1.0, v77
	v_fma_f32 v142, v142, v143, v198
	v_fma_f32 v197, v74, v195, v201
	v_cvt_pk_bf16_f32 v74, v142, v153
	v_cvt_pk_bf16_f32 v75, v196, v197
	s_nop 0
	v_lshlrev_b32_e32 v76, 16, v74
	v_and_b32_e32 v77, 0xffff0000, v74
	v_and_b32_e32 v216, 0xffff0000, v75
	v_sub_f32_e32 v76, v142, v76
	v_sub_f32_e32 v77, v153, v77
	v_lshlrev_b32_e32 v215, 16, v75
	v_sub_f32_e32 v216, v197, v216
	v_sub_f32_e32 v215, v196, v215
	v_cvt_pk_bf16_f32 v76, v76, v77
	v_cvt_pk_bf16_f32 v77, v215, v216
	v_mov_b32_e32 v216, 0
	v_mov_b32_e32 v215, v232
	v_cvt_pk_fp8_f32 v216, v142, v153
	v_cvt_pk_fp8_f32 v216, v196, v197 op_sel:[0,0,1]
	v_add_u32_e32 v215, 32, v215
	v_xor_b32_e32 v215, v215, v129
	v_lshl_add_u32 v142, v215, 4, v240
	v_add_u32_e32 v153, 0, v142
	ds_write_b64 v153, v[74:75]
	v_add_u32_e32 v74, s56, v142
	ds_write_b64 v74, v[76:77]
	v_lshl_add_u64 v[74:75], v[190:191], 0, v[78:79]
	global_store_dword v[74:75], v216, off offset:256
	v_mul_f32_e32 v74, v210, v213
	v_mul_f32_e32 v70, v74, v70
	v_fma_f32 v74, v70, v143, v198
	v_mul_f32_e32 v70, v211, v213
	v_mul_f32_e32 v70, v70, v71
	v_fma_f32 v75, v70, v152, v199
	v_mul_f32_e32 v70, v208, v213
	v_mul_f32_e32 v70, v70, v72
	v_fma_f32 v76, v70, v194, v200
	v_mul_f32_e32 v70, v209, v213
	v_mul_f32_e32 v70, v70, v73
	v_fmac_f32_e32 v201, v70, v195
	v_cvt_pk_bf16_f32 v70, v74, v75
	v_cvt_pk_bf16_f32 v71, v76, v201
	s_nop 0
	v_lshlrev_b32_e32 v72, 16, v70
	v_and_b32_e32 v73, 0xffff0000, v70
	v_and_b32_e32 v142, 0xffff0000, v71
	v_sub_f32_e32 v72, v74, v72
	v_sub_f32_e32 v73, v75, v73
	v_lshlrev_b32_e32 v77, 16, v71
	v_sub_f32_e32 v142, v201, v142
	v_sub_f32_e32 v77, v76, v77
	v_cvt_pk_bf16_f32 v72, v72, v73
	v_cvt_pk_bf16_f32 v73, v77, v142
	v_mov_b32_e32 v142, 0
	v_mov_b32_e32 v77, v232
	v_cvt_pk_fp8_f32 v142, v74, v75
	v_cvt_pk_fp8_f32 v142, v76, v201 op_sel:[0,0,1]
	v_add_u32_e32 v77, 32, v77
	v_xor_b32_e32 v77, v77, v235
	v_lshl_add_u32 v74, v77, 4, v241
	v_add_u32_e32 v75, 0, v74
	ds_write_b64 v75, v[70:71]
	v_add_u32_e32 v70, s56, v74
	ds_write_b64 v70, v[72:73]
	v_lshl_add_u64 v[70:71], v[192:193], 0, v[78:79]
	v_mov_b32_e32 v78, v128
	global_store_dword v[70:71], v142, off offset:256
	s_nop 0
	v_ashrrev_i32_e32 v79, 31, v78
	v_lshlrev_b64 v[70:71], 2, v[78:79]
	v_lshl_add_u64 v[74:75], v[70:71], 0, s[42:43]
	v_lshl_add_u64 v[70:71], s[28:29], 0, v[70:71]
	v_lshl_add_u64 v[76:77], v[68:69], 0, v[74:75]
	global_load_dwordx4 v[70:73], v[70:71], off offset:2048
	v_lshl_add_u64 v[142:143], v[116:117], 0, v[74:75]
	global_load_dwordx4 v[74:77], v[76:77], off
	s_nop 0
	global_load_dwordx4 v[194:197], v[142:143], off
	s_waitcnt vmcnt(2)
	v_mul_f32_e32 v126, v126, v70
	s_waitcnt vmcnt(1)
	v_add_f32_e32 v142, 1.0, v74
	v_mul_f32_e32 v74, v127, v214
	v_mul_f32_e32 v74, v74, v71
	v_add_f32_e32 v127, 1.0, v75
	s_waitcnt vmcnt(0)
	v_fma_f32 v143, v74, v127, v195
	v_mul_f32_e32 v74, v124, v214
	v_mul_f32_e32 v74, v74, v72
	v_add_f32_e32 v124, 1.0, v76
	v_fma_f32 v152, v74, v124, v196
	v_mul_f32_e32 v74, v125, v214
	v_mul_f32_e32 v74, v74, v73
	v_add_f32_e32 v125, 1.0, v77
	v_fma_f32 v126, v126, v142, v194
	v_fma_f32 v153, v74, v125, v197
	v_cvt_pk_bf16_f32 v74, v126, v143
	v_cvt_pk_bf16_f32 v75, v152, v153
	s_nop 0
	v_lshlrev_b32_e32 v76, 16, v74
	v_and_b32_e32 v77, 0xffff0000, v74
	v_and_b32_e32 v199, 0xffff0000, v75
	v_sub_f32_e32 v76, v126, v76
	v_sub_f32_e32 v77, v143, v77
	v_lshlrev_b32_e32 v198, 16, v75
	v_sub_f32_e32 v199, v153, v199
	v_sub_f32_e32 v198, v152, v198
	v_cvt_pk_bf16_f32 v76, v76, v77
	v_cvt_pk_bf16_f32 v77, v198, v199
	v_mov_b32_e32 v199, 0
	v_mov_b32_e32 v198, v232
	v_cvt_pk_fp8_f32 v199, v126, v143
	v_cvt_pk_fp8_f32 v199, v152, v153 op_sel:[0,0,1]
	v_add_u32_e32 v198, 64, v198
	v_xor_b32_e32 v198, v198, v129
	v_lshl_add_u32 v126, v198, 4, v240
	v_add_u32_e32 v143, 0, v126
	ds_write_b64 v143, v[74:75]
	v_add_u32_e32 v74, s56, v126
	ds_write_b64 v74, v[76:77]
	v_lshl_add_u64 v[74:75], v[190:191], 0, v[78:79]
	global_store_dword v[74:75], v199, off offset:512
	v_mul_f32_e32 v74, v202, v213
	v_mul_f32_e32 v70, v74, v70
	v_fma_f32 v74, v70, v142, v194
	v_mul_f32_e32 v70, v203, v213
	v_mul_f32_e32 v70, v70, v71
	v_fma_f32 v75, v70, v127, v195
	v_mul_f32_e32 v70, v98, v213
	v_mul_f32_e32 v70, v70, v72
	v_fma_f32 v76, v70, v124, v196
	v_mul_f32_e32 v70, v99, v213
	v_mul_f32_e32 v70, v70, v73
	v_fmac_f32_e32 v197, v70, v125
	v_cvt_pk_bf16_f32 v70, v74, v75
	v_cvt_pk_bf16_f32 v71, v76, v197
	s_nop 0
	v_lshlrev_b32_e32 v72, 16, v70
	v_and_b32_e32 v73, 0xffff0000, v70
	v_and_b32_e32 v98, 0xffff0000, v71
	v_sub_f32_e32 v72, v74, v72
	v_sub_f32_e32 v73, v75, v73
	v_lshlrev_b32_e32 v77, 16, v71
	v_sub_f32_e32 v98, v197, v98
	v_sub_f32_e32 v77, v76, v77
	v_cvt_pk_bf16_f32 v72, v72, v73
	v_cvt_pk_bf16_f32 v73, v77, v98
	v_mov_b32_e32 v98, 0
	v_mov_b32_e32 v77, v232
	v_cvt_pk_fp8_f32 v98, v74, v75
	v_cvt_pk_fp8_f32 v98, v76, v197 op_sel:[0,0,1]
	v_add_u32_e32 v77, 64, v77
	v_xor_b32_e32 v77, v77, v235
	v_lshl_add_u32 v74, v77, 4, v241
	v_add_u32_e32 v75, 0, v74
	ds_write_b64 v75, v[70:71]
	v_add_u32_e32 v70, s56, v74
	ds_write_b64 v70, v[72:73]
	v_lshl_add_u64 v[70:71], v[192:193], 0, v[78:79]
	v_mov_b32_e32 v78, v128
	global_store_dword v[70:71], v98, off offset:512
	s_nop 0
	v_ashrrev_i32_e32 v79, 31, v78
	v_lshlrev_b64 v[70:71], 2, v[78:79]
	v_lshl_add_u64 v[74:75], v[70:71], 0, s[44:45]
	v_lshl_add_u64 v[70:71], s[28:29], 0, v[70:71]
	v_lshl_add_u64 v[76:77], v[68:69], 0, v[74:75]
	global_load_dwordx4 v[70:73], v[70:71], off offset:3072
	v_lshl_add_u64 v[98:99], v[116:117], 0, v[74:75]
	global_load_dwordx4 v[74:77], v[76:77], off
	s_nop 0
	global_load_dwordx4 v[124:127], v[98:99], off
	v_mul_f32_e32 v98, v122, v214
	s_waitcnt vmcnt(2)
	v_mul_f32_e32 v98, v98, v70
	s_waitcnt vmcnt(1)
	v_add_f32_e32 v99, 1.0, v74
	v_mul_f32_e32 v74, v123, v214
	v_mul_f32_e32 v74, v74, v71
	v_add_f32_e32 v122, 1.0, v75
	s_waitcnt vmcnt(0)
	v_fma_f32 v123, v74, v122, v125
	v_mul_f32_e32 v74, v120, v214
	v_mul_f32_e32 v74, v74, v72
	v_add_f32_e32 v120, 1.0, v76
	v_fma_f32 v142, v74, v120, v126
	v_mul_f32_e32 v74, v121, v214
	v_mul_f32_e32 v74, v74, v73
	v_add_f32_e32 v121, 1.0, v77
	v_fma_f32 v98, v98, v99, v124
	v_fma_f32 v143, v74, v121, v127
	v_cvt_pk_bf16_f32 v74, v98, v123
	v_cvt_pk_bf16_f32 v75, v142, v143
	s_nop 0
	v_lshlrev_b32_e32 v76, 16, v74
	v_and_b32_e32 v77, 0xffff0000, v74
	v_and_b32_e32 v153, 0xffff0000, v75
	v_sub_f32_e32 v76, v98, v76
	v_sub_f32_e32 v77, v123, v77
	v_lshlrev_b32_e32 v152, 16, v75
	v_sub_f32_e32 v153, v143, v153
	v_sub_f32_e32 v152, v142, v152
	v_cvt_pk_bf16_f32 v76, v76, v77
	v_cvt_pk_bf16_f32 v77, v152, v153
	v_mov_b32_e32 v153, 0
	v_mov_b32_e32 v152, v232
	v_cvt_pk_fp8_f32 v153, v98, v123
	v_cvt_pk_fp8_f32 v153, v142, v143 op_sel:[0,0,1]
	v_add_u32_e32 v152, 0x60, v152
	v_xor_b32_e32 v152, v152, v129
	v_lshl_add_u32 v98, v152, 4, v240
	v_add_u32_e32 v123, 0, v98
	ds_write_b64 v123, v[74:75]
	v_add_u32_e32 v74, s56, v98
	ds_write_b64 v74, v[76:77]
	v_lshl_add_u64 v[74:75], v[190:191], 0, v[78:79]
	global_store_dword v[74:75], v153, off offset:768
	v_mul_f32_e32 v74, v94, v213
	v_mul_f32_e32 v70, v74, v70
	v_fma_f32 v74, v70, v99, v124
	v_mul_f32_e32 v70, v95, v213
	v_mul_f32_e32 v70, v70, v71
	v_fma_f32 v75, v70, v122, v125
	v_mul_f32_e32 v70, v90, v213
	v_mul_f32_e32 v70, v70, v72
	v_fma_f32 v76, v70, v120, v126
	v_mul_f32_e32 v70, v91, v213
	v_mul_f32_e32 v70, v70, v73
	v_fmac_f32_e32 v127, v70, v121
	v_cvt_pk_bf16_f32 v70, v74, v75
	v_cvt_pk_bf16_f32 v71, v76, v127
	v_mov_b64_e32 v[152:153], 0x1000
	v_lshlrev_b32_e32 v72, 16, v70
	v_and_b32_e32 v73, 0xffff0000, v70
	v_and_b32_e32 v90, 0xffff0000, v71
	v_sub_f32_e32 v72, v74, v72
	v_sub_f32_e32 v73, v75, v73
	v_lshlrev_b32_e32 v77, 16, v71
	v_sub_f32_e32 v90, v127, v90
	v_sub_f32_e32 v77, v76, v77
	v_cvt_pk_bf16_f32 v72, v72, v73
	v_cvt_pk_bf16_f32 v73, v77, v90
	v_mov_b32_e32 v90, 0
	v_mov_b32_e32 v77, v232
	v_cvt_pk_fp8_f32 v90, v74, v75
	v_cvt_pk_fp8_f32 v90, v76, v127 op_sel:[0,0,1]
	v_add_u32_e32 v77, 0x60, v77
	v_xor_b32_e32 v77, v77, v235
	v_lshl_add_u32 v74, v77, 4, v241
	v_add_u32_e32 v75, 0, v74
	ds_write_b64 v75, v[70:71]
	v_add_u32_e32 v70, s56, v74
	ds_write_b64 v70, v[72:73]
	v_lshl_add_u64 v[70:71], v[192:193], 0, v[78:79]
	global_store_dword v[70:71], v90, off offset:768
	v_mov_b32_e32 v90, v128
	s_nop 0
	v_ashrrev_i32_e32 v91, 31, v90
	v_lshl_add_u64 v[70:71], v[90:91], 2, v[152:153]
	v_lshl_add_u64 v[72:73], s[28:29], 0, v[70:71]
	global_load_dwordx4 v[76:79], v[72:73], off
	v_lshl_add_u64 v[72:73], v[68:69], 0, v[70:71]
	v_lshl_add_u64 v[74:75], v[116:117], 0, v[70:71]
	global_load_dwordx4 v[70:73], v[72:73], off
	s_nop 0
	global_load_dwordx4 v[120:123], v[74:75], off
	v_mul_f32_e32 v74, v112, v214
	s_waitcnt vmcnt(2)
	v_mul_f32_e32 v74, v74, v76
	s_waitcnt vmcnt(1)
	v_add_f32_e32 v94, 1.0, v70
	v_mul_f32_e32 v70, v113, v214
	v_mul_f32_e32 v70, v70, v77
	v_add_f32_e32 v95, 1.0, v71
	s_waitcnt vmcnt(0)
	v_fma_f32 v75, v70, v95, v121
	v_mul_f32_e32 v70, v114, v214
	v_mul_f32_e32 v70, v70, v78
	v_add_f32_e32 v98, 1.0, v72
	v_fma_f32 v74, v74, v94, v120
	v_fma_f32 v72, v70, v98, v122
	v_mul_f32_e32 v70, v115, v214
	v_mov_b32_e32 v115, 0
	v_cvt_pk_fp8_f32 v115, v74, v75
	v_mul_f32_e32 v70, v70, v79
	v_add_f32_e32 v99, 1.0, v73
	v_fma_f32 v73, v70, v99, v123
	v_cvt_pk_fp8_f32 v115, v72, v73 op_sel:[0,0,1]
	v_cvt_pk_bf16_f32 v70, v74, v75
	v_cvt_pk_bf16_f32 v71, v72, v73
	s_nop 0
	v_lshlrev_b32_e32 v112, 16, v70
	v_sub_f32_e32 v112, v74, v112
	v_and_b32_e32 v113, 0xffff0000, v70
	v_lshlrev_b32_e32 v114, 16, v71
	v_and_b32_e32 v74, 0xffff0000, v71
	v_sub_f32_e32 v113, v75, v113
	v_sub_f32_e32 v75, v72, v114
	v_sub_f32_e32 v114, v73, v74
	v_lshl_add_u64 v[72:73], v[190:191], 0, v[90:91]
	v_cvt_pk_bf16_f32 v74, v112, v113
	v_cvt_pk_bf16_f32 v75, v75, v114
	global_store_dword v[72:73], v115, off offset:1024
	v_mul_f32_e32 v72, v86, v213
	v_mul_f32_e32 v72, v72, v76
	v_fma_f32 v76, v72, v94, v120
	v_mul_f32_e32 v72, v87, v213
	v_mul_f32_e32 v72, v72, v77
	v_fma_f32 v77, v72, v95, v121
	v_mul_f32_e32 v72, v82, v213
	v_mov_b32_e32 v86, 0
	v_mul_f32_e32 v72, v72, v78
	v_cvt_pk_fp8_f32 v86, v76, v77
	v_fma_f32 v78, v72, v98, v122
	v_mul_f32_e32 v72, v83, v213
	v_mul_f32_e32 v72, v72, v79
	v_fmac_f32_e32 v123, v72, v99
	v_cvt_pk_fp8_f32 v86, v78, v123 op_sel:[0,0,1]
	v_cvt_pk_bf16_f32 v72, v76, v77
	v_cvt_pk_bf16_f32 v73, v78, v123
	s_nop 0
	v_lshlrev_b32_e32 v79, 16, v72
	v_sub_f32_e32 v79, v76, v79
	v_and_b32_e32 v82, 0xffff0000, v72
	v_lshlrev_b32_e32 v83, 16, v73
	v_and_b32_e32 v76, 0xffff0000, v73
	v_sub_f32_e32 v82, v77, v82
	v_sub_f32_e32 v77, v78, v83
	v_sub_f32_e32 v83, v123, v76
	v_cvt_pk_bf16_f32 v76, v79, v82
	v_lshl_add_u64 v[78:79], v[192:193], 0, v[90:91]
	v_cvt_pk_bf16_f32 v77, v77, v83
	global_store_dword v[78:79], v86, off offset:1024
	v_mov_b32_e32 v86, v128
	s_nop 0
	v_ashrrev_i32_e32 v87, 31, v86
	v_lshl_add_u64 v[78:79], v[86:87], 2, v[144:145]
	v_lshl_add_u64 v[82:83], s[28:29], 0, v[78:79]
	global_load_dwordx4 v[112:115], v[82:83], off
	v_lshl_add_u64 v[82:83], v[68:69], 0, v[78:79]
	v_lshl_add_u64 v[78:79], v[116:117], 0, v[78:79]
	global_load_dwordx4 v[120:123], v[82:83], off
	global_load_dwordx4 v[124:127], v[78:79], off
	v_mul_f32_e32 v78, v108, v214
	s_waitcnt vmcnt(2)
	v_mul_f32_e32 v78, v78, v112
	v_mul_f32_e32 v84, v84, v112
	s_waitcnt vmcnt(1)
	v_add_f32_e32 v94, 1.0, v120
	s_waitcnt vmcnt(0)
	v_fma_f32 v82, v78, v94, v124
	v_mul_f32_e32 v78, v109, v214
	v_mul_f32_e32 v78, v78, v113
	v_add_f32_e32 v95, 1.0, v121
	v_fma_f32 v83, v78, v95, v125
	v_mul_f32_e32 v78, v110, v214
	v_mul_f32_e32 v78, v78, v114
	v_add_f32_e32 v98, 1.0, v122
	v_fma_f32 v90, v78, v98, v126
	v_mul_f32_e32 v78, v111, v214
	v_mov_b32_e32 v111, 0
	v_cvt_pk_fp8_f32 v111, v82, v83
	v_mul_f32_e32 v78, v78, v115
	v_add_f32_e32 v99, 1.0, v123
	v_fma_f32 v91, v78, v99, v127
	v_cvt_pk_fp8_f32 v111, v90, v91 op_sel:[0,0,1]
	v_cvt_pk_bf16_f32 v78, v82, v83
	v_cvt_pk_bf16_f32 v79, v90, v91
	v_mul_f32_e32 v85, v85, v113
	v_lshlrev_b32_e32 v108, 16, v78
	v_sub_f32_e32 v108, v82, v108
	v_and_b32_e32 v109, 0xffff0000, v78
	v_lshlrev_b32_e32 v110, 16, v79
	v_and_b32_e32 v82, 0xffff0000, v79
	v_sub_f32_e32 v109, v83, v109
	v_sub_f32_e32 v83, v90, v110
	v_sub_f32_e32 v110, v91, v82
	v_lshl_add_u64 v[90:91], v[190:191], 0, v[86:87]
	v_mul_f32_e32 v80, v80, v114
	v_cvt_pk_bf16_f32 v82, v108, v109
	v_cvt_pk_bf16_f32 v83, v83, v110
	global_store_dword v[90:91], v111, off offset:1280
	v_fma_f32 v84, v84, v94, v124
	v_fma_f32 v85, v85, v95, v125
	v_fma_f32 v90, v80, v98, v126
	v_mov_b32_e32 v98, 0
	v_cvt_pk_fp8_f32 v98, v84, v85
	v_mul_f32_e32 v80, v81, v213
	v_mul_f32_e32 v80, v80, v115
	v_fmac_f32_e32 v127, v80, v99
	v_cvt_pk_fp8_f32 v98, v90, v127 op_sel:[0,0,1]
	v_cvt_pk_bf16_f32 v80, v84, v85
	v_cvt_pk_bf16_f32 v81, v90, v127
	v_lshl_add_u64 v[86:87], v[192:193], 0, v[86:87]
	v_lshlrev_b32_e32 v91, 16, v80
	v_and_b32_e32 v94, 0xffff0000, v80
	v_sub_f32_e32 v91, v84, v91
	v_sub_f32_e32 v94, v85, v94
	v_lshlrev_b32_e32 v95, 16, v81
	v_and_b32_e32 v84, 0xffff0000, v81
	v_sub_f32_e32 v85, v90, v95
	v_sub_f32_e32 v95, v127, v84
	v_cvt_pk_bf16_f32 v84, v91, v94
	v_mov_b32_e32 v94, v128
	v_cvt_pk_bf16_f32 v85, v85, v95
	global_store_dword v[86:87], v98, off offset:1280
	v_mov_b32_e32 v126, v128
	v_ashrrev_i32_e32 v95, 31, v94
	v_lshl_add_u64 v[86:87], v[94:95], 2, v[146:147]
	v_lshl_add_u64 v[90:91], s[28:29], 0, v[86:87]
	global_load_dwordx4 v[108:111], v[90:91], off
	v_lshl_add_u64 v[90:91], v[68:69], 0, v[86:87]
	v_lshl_add_u64 v[86:87], v[116:117], 0, v[86:87]
	global_load_dwordx4 v[112:115], v[90:91], off
	global_load_dwordx4 v[120:123], v[86:87], off
	v_mul_f32_e32 v86, v104, v214
	s_waitcnt vmcnt(2)
	v_mul_f32_e32 v86, v86, v108
	v_mul_f32_e32 v92, v92, v108
	s_waitcnt vmcnt(1)
	v_add_f32_e32 v104, 1.0, v112
	s_waitcnt vmcnt(0)
	v_fma_f32 v90, v86, v104, v120
	v_mul_f32_e32 v86, v105, v214
	v_mul_f32_e32 v86, v86, v109
	v_add_f32_e32 v105, 1.0, v113
	v_fma_f32 v91, v86, v105, v121
	v_mul_f32_e32 v86, v106, v214
	v_mul_f32_e32 v86, v86, v110
	v_add_f32_e32 v106, 1.0, v114
	v_fma_f32 v98, v86, v106, v122
	v_mul_f32_e32 v86, v107, v214
	v_add_f32_e32 v107, 1.0, v115
	v_mov_b32_e32 v115, 0
	v_cvt_pk_fp8_f32 v115, v90, v91
	v_mul_f32_e32 v86, v86, v111
	v_fma_f32 v99, v86, v107, v123
	v_cvt_pk_bf16_f32 v86, v90, v91
	v_cvt_pk_fp8_f32 v115, v98, v99 op_sel:[0,0,1]
	v_lshlrev_b32_e32 v112, 16, v86
	v_cvt_pk_bf16_f32 v87, v98, v99
	v_sub_f32_e32 v112, v90, v112
	v_and_b32_e32 v113, 0xffff0000, v86
	v_lshlrev_b32_e32 v114, 16, v87
	v_and_b32_e32 v90, 0xffff0000, v87
	v_sub_f32_e32 v113, v91, v113
	v_sub_f32_e32 v91, v98, v114
	v_sub_f32_e32 v114, v99, v90
	v_lshl_add_u64 v[98:99], v[190:191], 0, v[94:95]
	v_mul_f32_e32 v93, v93, v109
	v_mul_f32_e32 v88, v88, v110
	v_cvt_pk_bf16_f32 v90, v112, v113
	v_cvt_pk_bf16_f32 v91, v91, v114
	global_store_dword v[98:99], v115, off offset:1536
	v_fma_f32 v92, v92, v104, v120
	v_fma_f32 v93, v93, v105, v121
	v_fma_f32 v98, v88, v106, v122
	v_mov_b32_e32 v106, 0
	v_cvt_pk_fp8_f32 v106, v92, v93
	v_mul_f32_e32 v88, v89, v213
	v_mul_f32_e32 v88, v88, v111
	v_fmac_f32_e32 v123, v88, v107
	v_cvt_pk_fp8_f32 v106, v98, v123 op_sel:[0,0,1]
	v_cvt_pk_bf16_f32 v88, v92, v93
	v_cvt_pk_bf16_f32 v89, v98, v123
	v_lshl_add_u64 v[94:95], v[192:193], 0, v[94:95]
	v_lshlrev_b32_e32 v99, 16, v88
	v_and_b32_e32 v104, 0xffff0000, v88
	v_lshlrev_b32_e32 v105, 16, v89
	v_sub_f32_e32 v99, v92, v99
	v_sub_f32_e32 v104, v93, v104
	v_sub_f32_e32 v93, v98, v105
	v_and_b32_e32 v92, 0xffff0000, v89
	v_mov_b32_e32 v120, v128
	v_sub_f32_e32 v105, v123, v92
	v_cvt_pk_bf16_f32 v92, v99, v104
	v_cvt_pk_bf16_f32 v93, v93, v105
	global_store_dword v[94:95], v106, off offset:1536
	v_mov_b32_e32 v123, 0
	v_ashrrev_i32_e32 v121, 31, v120
	v_lshl_add_u64 v[94:95], v[120:121], 2, v[148:149]
	v_lshl_add_u64 v[98:99], s[28:29], 0, v[94:95]
	global_load_dwordx4 v[104:107], v[98:99], off
	v_lshl_add_u64 v[98:99], v[68:69], 0, v[94:95]
	v_lshl_add_u64 v[94:95], v[116:117], 0, v[94:95]
	global_load_dwordx4 v[108:111], v[98:99], off
	global_load_dwordx4 v[112:115], v[94:95], off
	v_mul_f32_e32 v94, v100, v214
	s_waitcnt vmcnt(2)
	v_mul_f32_e32 v94, v94, v104
	v_mul_f32_e32 v96, v96, v106
	s_waitcnt vmcnt(1)
	v_add_f32_e32 v108, 1.0, v108
	s_waitcnt vmcnt(0)
	v_fma_f32 v98, v94, v108, v112
	v_mul_f32_e32 v94, v101, v214
	v_mul_f32_e32 v94, v94, v105
	v_add_f32_e32 v109, 1.0, v109
	v_fma_f32 v99, v94, v109, v113
	v_mul_f32_e32 v94, v102, v214
	v_mul_f32_e32 v94, v94, v106
	v_add_f32_e32 v102, 1.0, v110
	v_cvt_pk_fp8_f32 v123, v98, v99
	v_fma_f32 v100, v94, v102, v114
	v_mul_f32_e32 v94, v103, v214
	v_mul_f32_e32 v94, v94, v107
	v_add_f32_e32 v103, 1.0, v111
	v_fma_f32 v101, v94, v103, v115
	v_cvt_pk_fp8_f32 v123, v100, v101 op_sel:[0,0,1]
	v_cvt_pk_bf16_f32 v94, v98, v99
	v_cvt_pk_bf16_f32 v95, v100, v101
	v_mov_b32_e32 v106, 0
	v_lshlrev_b32_e32 v110, 16, v94
	v_sub_f32_e32 v110, v98, v110
	v_and_b32_e32 v111, 0xffff0000, v94
	v_lshlrev_b32_e32 v122, 16, v95
	v_and_b32_e32 v98, 0xffff0000, v95
	v_sub_f32_e32 v111, v99, v111
	v_sub_f32_e32 v99, v100, v122
	v_sub_f32_e32 v122, v101, v98
	v_lshl_add_u64 v[100:101], v[190:191], 0, v[120:121]
	v_cvt_pk_bf16_f32 v98, v110, v111
	v_cvt_pk_bf16_f32 v99, v99, v122
	global_store_dword v[100:101], v123, off offset:1792
	v_mul_f32_e32 v100, v118, v213
	v_mul_f32_e32 v101, v119, v213
	v_mul_f32_e32 v100, v100, v104
	v_mul_f32_e32 v101, v101, v105
	v_fma_f32 v100, v100, v108, v112
	v_fma_f32 v101, v101, v109, v113
	v_cvt_pk_fp8_f32 v106, v100, v101
	v_fma_f32 v102, v96, v102, v114
	v_mul_f32_e32 v96, v97, v213
	v_mul_f32_e32 v96, v96, v107
	v_fmac_f32_e32 v115, v96, v103
	v_cvt_pk_fp8_f32 v106, v102, v115 op_sel:[0,0,1]
	v_cvt_pk_bf16_f32 v96, v100, v101
	v_cvt_pk_bf16_f32 v97, v102, v115
	v_and_b32_e32 v107, 0xffff0000, v187
	v_lshlrev_b32_e32 v103, 16, v96
	v_sub_f32_e32 v103, v100, v103
	v_and_b32_e32 v104, 0xffff0000, v96
	v_lshlrev_b32_e32 v105, 16, v97
	v_and_b32_e32 v100, 0xffff0000, v97
	v_sub_f32_e32 v104, v101, v104
	v_sub_f32_e32 v101, v102, v105
	v_sub_f32_e32 v105, v115, v100
	v_cvt_pk_bf16_f32 v100, v103, v104
	v_lshl_add_u64 v[102:103], v[192:193], 0, v[120:121]
	v_cvt_pk_bf16_f32 v101, v101, v105
	global_store_dword v[102:103], v106, off offset:1792
	v_lshlrev_b64 v[102:103], 12, v[184:185]
	v_lshlrev_b32_e32 v106, 16, v187
	v_lshlrev_b32_e32 v104, 16, v186
	v_and_b32_e32 v105, 0xffff0000, v186
	v_pk_add_f32 v[66:67], v[66:67], v[106:107]
	v_lshl_add_u64 v[106:107], v[130:131], 0, v[102:103]
	v_lshl_add_u64 v[102:103], s[76:77], 0, v[102:103]
	v_pk_add_f32 v[64:65], v[64:65], v[104:105]
	v_lshl_add_u64 v[102:103], v[102:103], 0, v[138:139]
	v_cvt_pk_bf16_f32 v104, v64, v65
	v_cvt_pk_bf16_f32 v105, v66, v67
	global_store_dwordx2 v[106:107], v[104:105], off
	v_lshlrev_b32_e32 v104, 16, v188
	v_and_b32_e32 v105, 0xffff0000, v188
	v_lshlrev_b32_e32 v106, 16, v189
	v_and_b32_e32 v107, 0xffff0000, v189
	v_add_co_u32_e32 v102, vcc, s52, v102
	v_pk_add_f32 v[62:63], v[62:63], v[106:107]
	v_pk_add_f32 v[60:61], v[60:61], v[104:105]
	v_addc_co_u32_e32 v103, vcc, 0, v103, vcc
	v_cvt_pk_bf16_f32 v104, v60, v61
	v_cvt_pk_bf16_f32 v105, v62, v63
	global_store_dwordx2 v[102:103], v[104:105], off offset:512
	v_lshlrev_b32_e32 v104, 16, v182
	v_and_b32_e32 v105, 0xffff0000, v182
	v_lshlrev_b32_e32 v106, 16, v183
	v_and_b32_e32 v107, 0xffff0000, v183
	v_pk_add_f32 v[58:59], v[58:59], v[106:107]
	v_pk_add_f32 v[56:57], v[56:57], v[104:105]
	v_lshlrev_b32_e32 v106, 16, v181
	v_cvt_pk_bf16_f32 v104, v56, v57
	v_cvt_pk_bf16_f32 v105, v58, v59
	global_store_dwordx2 v[102:103], v[104:105], off offset:1024
	v_lshlrev_b32_e32 v104, 16, v180
	v_and_b32_e32 v105, 0xffff0000, v180
	v_and_b32_e32 v107, 0xffff0000, v181
	v_pk_add_f32 v[54:55], v[54:55], v[106:107]
	v_pk_add_f32 v[52:53], v[52:53], v[104:105]
	v_lshlrev_b32_e32 v106, 16, v179
	v_cvt_pk_bf16_f32 v104, v52, v53
	v_cvt_pk_bf16_f32 v105, v54, v55
	global_store_dwordx2 v[102:103], v[104:105], off offset:1536
	v_lshlrev_b32_e32 v104, 16, v178
	v_and_b32_e32 v105, 0xffff0000, v178
	v_and_b32_e32 v107, 0xffff0000, v179
	v_pk_add_f32 v[50:51], v[50:51], v[106:107]
	v_pk_add_f32 v[48:49], v[48:49], v[104:105]
	v_lshlrev_b32_e32 v106, 16, v177
	v_cvt_pk_bf16_f32 v104, v48, v49
	v_cvt_pk_bf16_f32 v105, v50, v51
	global_store_dwordx2 v[102:103], v[104:105], off offset:2048
	v_lshlrev_b32_e32 v104, 16, v176
	v_and_b32_e32 v105, 0xffff0000, v176
	v_and_b32_e32 v107, 0xffff0000, v177
	v_pk_add_f32 v[44:45], v[44:45], v[104:105]
	v_pk_add_f32 v[46:47], v[46:47], v[106:107]
	v_cvt_pk_bf16_f32 v104, v44, v45
	v_mov_b32_e32 v106, v49
	v_cvt_pk_bf16_f32 v105, v46, v47
	v_mov_b32_e32 v107, v45
	global_store_dwordx2 v[102:103], v[104:105], off offset:2560
	v_mov_b32_e32 v104, v48
	v_mov_b32_e32 v105, v44
	v_pk_mul_f32 v[106:107], v[106:107], v[106:107]
	v_lshlrev_b32_e32 v108, 16, v175
	v_pk_fma_f32 v[104:105], v[104:105], v[104:105], v[106:107]
	v_mov_b32_e32 v106, v50
	v_mov_b32_e32 v107, v46
	v_pk_fma_f32 v[104:105], v[106:107], v[106:107], v[104:105]
	v_mov_b32_e32 v106, v51
	v_mov_b32_e32 v107, v47
	v_pk_fma_f32 v[106:107], v[106:107], v[106:107], v[104:105]
	v_lshlrev_b32_e32 v104, 16, v174
	v_and_b32_e32 v105, 0xffff0000, v174
	v_and_b32_e32 v109, 0xffff0000, v175
	v_pk_add_f32 v[42:43], v[42:43], v[108:109]
	v_pk_add_f32 v[40:41], v[40:41], v[104:105]
	v_lshlrev_b32_e32 v108, 16, v173
	v_cvt_pk_bf16_f32 v104, v40, v41
	v_cvt_pk_bf16_f32 v105, v42, v43
	global_store_dwordx2 v[102:103], v[104:105], off offset:3072
	v_lshlrev_b32_e32 v104, 16, v172
	v_and_b32_e32 v105, 0xffff0000, v172
	v_and_b32_e32 v109, 0xffff0000, v173
	v_pk_add_f32 v[38:39], v[38:39], v[108:109]
	v_pk_add_f32 v[36:37], v[36:37], v[104:105]
	v_lshlrev_b64 v[110:111], 12, v[166:167]
	v_cvt_pk_bf16_f32 v104, v36, v37
	v_cvt_pk_bf16_f32 v105, v38, v39
	global_store_dwordx2 v[102:103], v[104:105], off offset:3584
	v_mov_b32_e32 v104, v41
	v_mov_b32_e32 v105, v37
	v_mov_b32_e32 v102, v40
	v_mov_b32_e32 v103, v36
	v_pk_mul_f32 v[104:105], v[104:105], v[104:105]
	v_mov_b32_e32 v113, v65
	v_pk_fma_f32 v[102:103], v[102:103], v[102:103], v[104:105]
	v_mov_b32_e32 v104, v42
	v_mov_b32_e32 v105, v38
	v_pk_fma_f32 v[102:103], v[104:105], v[104:105], v[102:103]
	v_mov_b32_e32 v104, v43
	v_mov_b32_e32 v105, v39
	v_pk_fma_f32 v[108:109], v[104:105], v[104:105], v[102:103]
	v_lshlrev_b32_e32 v104, 16, v168
	v_and_b32_e32 v105, 0xffff0000, v168
	v_lshlrev_b32_e32 v102, 16, v169
	v_and_b32_e32 v103, 0xffff0000, v169
	v_pk_add_f32 v[102:103], v[34:35], v[102:103]
	v_pk_add_f32 v[104:105], v[32:33], v[104:105]
	v_lshl_add_u64 v[34:35], v[130:131], 0, v[110:111]
	v_cvt_pk_bf16_f32 v32, v104, v105
	v_cvt_pk_bf16_f32 v33, v102, v103
	global_store_dwordx2 v[34:35], v[32:33], off
	v_lshlrev_b32_e32 v32, 16, v171
	v_and_b32_e32 v33, 0xffff0000, v171
	v_pk_add_f32 v[32:33], v[30:31], v[32:33]
	v_lshl_add_u64 v[30:31], s[76:77], 0, v[110:111]
	v_lshl_add_u64 v[30:31], v[30:31], 0, v[138:139]
	v_lshlrev_b32_e32 v34, 16, v170
	v_and_b32_e32 v35, 0xffff0000, v170
	v_add_co_u32_e32 v110, vcc, s52, v30
	v_pk_add_f32 v[34:35], v[28:29], v[34:35]
	s_nop 0
	v_addc_co_u32_e32 v111, vcc, 0, v31, vcc
	v_cvt_pk_bf16_f32 v28, v34, v35
	v_cvt_pk_bf16_f32 v29, v32, v33
	global_store_dwordx2 v[110:111], v[28:29], off offset:512
	v_lshlrev_b32_e32 v30, 16, v164
	v_and_b32_e32 v31, 0xffff0000, v164
	v_lshlrev_b32_e32 v28, 16, v165
	v_and_b32_e32 v29, 0xffff0000, v165
	v_pk_add_f32 v[28:29], v[26:27], v[28:29]
	v_pk_add_f32 v[30:31], v[24:25], v[30:31]
	v_lshlrev_b32_e32 v26, 16, v163
	v_cvt_pk_bf16_f32 v24, v30, v31
	v_cvt_pk_bf16_f32 v25, v28, v29
	global_store_dwordx2 v[110:111], v[24:25], off offset:1024
	v_lshlrev_b32_e32 v24, 16, v162
	v_and_b32_e32 v25, 0xffff0000, v162
	v_and_b32_e32 v27, 0xffff0000, v163
	v_pk_add_f32 v[22:23], v[22:23], v[26:27]
	v_pk_add_f32 v[26:27], v[20:21], v[24:25]
	v_lshlrev_b32_e32 v24, 16, v161
	v_cvt_pk_bf16_f32 v20, v26, v27
	v_cvt_pk_bf16_f32 v21, v22, v23
	global_store_dwordx2 v[110:111], v[20:21], off offset:1536
	v_lshlrev_b32_e32 v20, 16, v160
	v_and_b32_e32 v21, 0xffff0000, v160
	v_and_b32_e32 v25, 0xffff0000, v161
	v_pk_add_f32 v[18:19], v[18:19], v[24:25]
	v_pk_add_f32 v[16:17], v[16:17], v[20:21]
	v_lshlrev_b32_e32 v24, 16, v159
	v_cvt_pk_bf16_f32 v20, v16, v17
	v_cvt_pk_bf16_f32 v21, v18, v19
	global_store_dwordx2 v[110:111], v[20:21], off offset:2048
	v_lshlrev_b32_e32 v20, 16, v158
	v_and_b32_e32 v21, 0xffff0000, v158
	v_and_b32_e32 v25, 0xffff0000, v159
	v_pk_add_f32 v[12:13], v[12:13], v[20:21]
	v_pk_add_f32 v[14:15], v[14:15], v[24:25]
	v_cvt_pk_bf16_f32 v20, v12, v13
	v_mov_b32_e32 v24, v17
	v_cvt_pk_bf16_f32 v21, v14, v15
	v_mov_b32_e32 v25, v13
	global_store_dwordx2 v[110:111], v[20:21], off offset:2560
	v_mov_b32_e32 v20, v16
	v_mov_b32_e32 v21, v12
	v_pk_mul_f32 v[24:25], v[24:25], v[24:25]
	v_mov_b32_e32 v112, v105
	v_pk_fma_f32 v[20:21], v[20:21], v[20:21], v[24:25]
	v_mov_b32_e32 v24, v18
	v_mov_b32_e32 v25, v14
	v_pk_fma_f32 v[20:21], v[24:25], v[24:25], v[20:21]
	v_mov_b32_e32 v24, v19
	v_mov_b32_e32 v25, v15
	v_pk_fma_f32 v[20:21], v[24:25], v[24:25], v[20:21]
	v_mov_b32_e32 v24, v104
	v_mov_b32_e32 v25, v64
	v_pk_mul_f32 v[112:113], v[112:113], v[112:113]
	v_mov_b32_e32 v114, v35
	v_pk_fma_f32 v[24:25], v[24:25], v[24:25], v[112:113]
	v_mov_b32_e32 v112, v102
	v_mov_b32_e32 v113, v66
	v_pk_fma_f32 v[24:25], v[112:113], v[112:113], v[24:25]
	v_mov_b32_e32 v112, v103
	v_mov_b32_e32 v113, v67
	v_mov_b32_e32 v115, v61
	v_pk_fma_f32 v[24:25], v[112:113], v[112:113], v[24:25]
	v_mov_b32_e32 v112, v34
	v_mov_b32_e32 v113, v60
	v_pk_mul_f32 v[114:115], v[114:115], v[114:115]
	v_lshlrev_b32_e32 v118, 16, v155
	v_pk_fma_f32 v[112:113], v[112:113], v[112:113], v[114:115]
	v_mov_b32_e32 v114, v32
	v_mov_b32_e32 v115, v62
	v_pk_fma_f32 v[112:113], v[114:115], v[114:115], v[112:113]
	v_mov_b32_e32 v114, v33
	v_mov_b32_e32 v115, v63
	v_pk_fma_f32 v[112:113], v[114:115], v[114:115], v[112:113]
	v_mov_b32_e32 v114, v31
	v_mov_b32_e32 v115, v57
	v_pk_add_f32 v[24:25], v[24:25], v[112:113]
	v_mov_b32_e32 v112, v30
	v_mov_b32_e32 v113, v56
	v_pk_mul_f32 v[114:115], v[114:115], v[114:115]
	v_and_b32_e32 v119, 0xffff0000, v155
	v_pk_fma_f32 v[112:113], v[112:113], v[112:113], v[114:115]
	v_mov_b32_e32 v114, v28
	v_mov_b32_e32 v115, v58
	v_pk_fma_f32 v[112:113], v[114:115], v[114:115], v[112:113]
	v_mov_b32_e32 v114, v29
	v_mov_b32_e32 v115, v59
	v_pk_fma_f32 v[112:113], v[114:115], v[114:115], v[112:113]
	v_mov_b32_e32 v114, v27
	v_mov_b32_e32 v115, v53
	v_pk_add_f32 v[24:25], v[24:25], v[112:113]
	v_mov_b32_e32 v112, v26
	v_mov_b32_e32 v113, v52
	v_pk_mul_f32 v[114:115], v[114:115], v[114:115]
	v_pk_add_f32 v[10:11], v[10:11], v[118:119]
	v_pk_fma_f32 v[112:113], v[112:113], v[112:113], v[114:115]
	v_mov_b32_e32 v114, v22
	v_mov_b32_e32 v115, v54
	v_pk_fma_f32 v[112:113], v[114:115], v[114:115], v[112:113]
	v_mov_b32_e32 v114, v23
	v_mov_b32_e32 v115, v55
	v_pk_fma_f32 v[112:113], v[114:115], v[114:115], v[112:113]
	v_lshlrev_b32_e32 v118, 16, v157
	v_pk_add_f32 v[24:25], v[24:25], v[112:113]
	v_lshlrev_b32_e32 v112, 16, v154
	v_and_b32_e32 v113, 0xffff0000, v154
	v_pk_add_f32 v[8:9], v[8:9], v[112:113]
	v_and_b32_e32 v119, 0xffff0000, v157
	v_cvt_pk_bf16_f32 v112, v8, v9
	v_cvt_pk_bf16_f32 v113, v10, v11
	global_store_dwordx2 v[110:111], v[112:113], off offset:3072
	v_lshlrev_b32_e32 v112, 16, v156
	v_and_b32_e32 v113, 0xffff0000, v156
	v_pk_add_f32 v[6:7], v[6:7], v[118:119]
	v_pk_add_f32 v[4:5], v[4:5], v[112:113]
	v_mov_b32_e32 v114, v20
	v_cvt_pk_bf16_f32 v112, v4, v5
	v_cvt_pk_bf16_f32 v113, v6, v7
	global_store_dwordx2 v[110:111], v[112:113], off offset:3584
	v_mov_b32_e32 v115, v106
	v_ashrrev_i32_e32 v127, 31, v126
	v_lshlrev_b64 v[118:119], 2, v[126:127]
	v_lshl_add_u64 v[110:111], s[28:29], 0, v[118:119]
	global_load_dwordx4 v[110:113], v[110:111], off
	v_lshl_add_u64 v[120:121], v[68:69], 0, v[118:119]
	v_lshl_add_u64 v[122:123], v[116:117], 0, v[118:119]
	global_load_dwordx4 v[118:121], v[120:121], off
	s_nop 0
	global_load_dwordx4 v[122:125], v[122:123], off
	v_mov_b32_e32 v142, v9
	v_mov_b32_e32 v143, v5
	v_pk_add_f32 v[24:25], v[24:25], v[114:115]
	v_mov_b32_e32 v114, v8
	v_mov_b32_e32 v115, v4
	v_pk_mul_f32 v[142:143], v[142:143], v[142:143]
	v_mov_b32_e32 v106, v21
	v_pk_fma_f32 v[114:115], v[114:115], v[114:115], v[142:143]
	v_mov_b32_e32 v142, v10
	v_mov_b32_e32 v143, v6
	v_pk_fma_f32 v[114:115], v[142:143], v[142:143], v[114:115]
	v_mov_b32_e32 v142, v11
	v_mov_b32_e32 v143, v7
	v_pk_fma_f32 v[114:115], v[142:143], v[142:143], v[114:115]
	v_pk_add_f32 v[20:21], v[24:25], v[106:107]
	v_mov_b32_e32 v24, v114
	v_mov_b32_e32 v25, v108
	v_pk_add_f32 v[20:21], v[20:21], v[24:25]
	v_mov_b32_e32 v108, v115
	v_pk_add_f32 v[20:21], v[20:21], v[108:109]
	ds_bpermute_b32 v25, v3, v21
	ds_bpermute_b32 v24, v3, v20
	s_waitcnt lgkmcnt(0)
	v_pk_add_f32 v[20:21], v[20:21], v[24:25]
	ds_bpermute_b32 v25, v204, v21
	ds_bpermute_b32 v24, v204, v20
	s_waitcnt lgkmcnt(0)
	v_pk_add_f32 v[20:21], v[20:21], v[24:25]
	ds_bpermute_b32 v25, v205, v21
	ds_bpermute_b32 v24, v205, v20
	s_waitcnt lgkmcnt(0)
	v_pk_add_f32 v[20:21], v[20:21], v[24:25]
	ds_bpermute_b32 v25, v206, v21
	ds_bpermute_b32 v24, v206, v20
	s_waitcnt lgkmcnt(0)
	v_pk_add_f32 v[20:21], v[20:21], v[24:25]
	ds_bpermute_b32 v25, v207, v21
	ds_bpermute_b32 v24, v207, v20
	s_waitcnt lgkmcnt(0)
	v_pk_add_f32 v[20:21], v[20:21], v[24:25]
	ds_bpermute_b32 v25, v212, v21
	ds_bpermute_b32 v24, v212, v20
	s_waitcnt lgkmcnt(0)
	v_pk_add_f32 v[20:21], v[20:21], v[24:25]
	s_nop 0
	v_pk_fma_f32 v[20:21], v[20:21], s[38:39], v[140:141] op_sel_hi:[1,0,0]
	s_nop 0
	v_mul_f32_e32 v3, 0x4b800000, v21
	v_cmp_gt_f32_e32 vcc, s53, v21
	v_cmp_gt_f32_e64 s[10:11], s53, v20
	s_nop 0
	v_cndmask_b32_e32 v3, v21, v3, vcc
	v_mul_f32_e32 v21, 0x4b800000, v20
	v_rsq_f32_e32 v3, v3
	v_cndmask_b32_e64 v20, v20, v21, s[10:11]
	v_rsq_f32_e32 v20, v20
	v_mul_f32_e32 v21, 0x45800000, v3
	v_cndmask_b32_e32 v106, v3, v21, vcc
	v_mul_f32_e32 v3, 0x45800000, v20
	v_cndmask_b32_e64 v3, v20, v3, s[10:11]
	v_mul_f32_e32 v20, v64, v106
	s_waitcnt vmcnt(2)
	v_mul_f32_e32 v20, v20, v110
	s_waitcnt vmcnt(1)
	v_add_f32_e32 v64, 1.0, v118
	s_waitcnt vmcnt(0)
	v_fma_f32 v107, v20, v64, v122
	v_mul_f32_e32 v20, v65, v106
	v_mul_f32_e32 v20, v20, v111
	v_add_f32_e32 v65, 1.0, v119
	v_fma_f32 v108, v20, v65, v123
	v_mul_f32_e32 v20, v66, v106
	v_mul_f32_e32 v20, v20, v112
	v_add_f32_e32 v66, 1.0, v120
	v_fma_f32 v109, v20, v66, v124
	v_mul_f32_e32 v20, v67, v106
	v_mul_f32_e32 v20, v20, v113
	v_add_f32_e32 v67, 1.0, v121
	v_fma_f32 v114, v20, v67, v125
	v_cvt_pk_bf16_f32 v20, v107, v108
	v_cvt_pk_bf16_f32 v21, v109, v114
	v_mul_f32_e32 v60, v60, v106
	v_lshlrev_b32_e32 v24, 16, v20
	v_and_b32_e32 v25, 0xffff0000, v20
	v_and_b32_e32 v118, 0xffff0000, v21
	v_sub_f32_e32 v24, v107, v24
	v_sub_f32_e32 v25, v108, v25
	v_lshlrev_b32_e32 v115, 16, v21
	v_sub_f32_e32 v118, v114, v118
	v_sub_f32_e32 v115, v109, v115
	v_cvt_pk_bf16_f32 v24, v24, v25
	v_cvt_pk_bf16_f32 v25, v115, v118
	v_mov_b32_e32 v118, 0
	v_mov_b32_e32 v115, v232
	v_cvt_pk_fp8_f32 v118, v107, v108
	v_mul_f32_e32 v34, v34, v3
	v_xor_b32_e32 v115, v115, v236
	v_lshl_add_u32 v115, v115, 4, v242
	v_add_u32_e32 v107, 0, v115
	v_cvt_pk_fp8_f32 v118, v109, v114 op_sel:[0,0,1]
	ds_write_b64 v107, v[20:21]
	v_add_u32_e32 v20, s56, v115
	ds_write_b64 v20, v[24:25]
	v_lshl_add_u64 v[20:21], s[24:25], 0, v[150:151]
	v_lshl_add_u64 v[24:25], v[20:21], 0, v[126:127]
	global_store_dword v[24:25], v118, off
	v_mul_f32_e32 v24, v104, v3
	v_mul_f32_e32 v24, v110, v24
	v_fma_f32 v104, v64, v24, v122
	v_mul_f32_e32 v24, v105, v3
	v_mul_f32_e32 v24, v111, v24
	v_fma_f32 v105, v65, v24, v123
	v_mul_f32_e32 v24, v102, v3
	v_mul_f32_e32 v24, v112, v24
	v_fma_f32 v66, v66, v24, v124
	v_mul_f32_e32 v24, v103, v3
	v_mul_f32_e32 v24, v113, v24
	v_fmac_f32_e32 v125, v67, v24
	v_cvt_pk_bf16_f32 v24, v104, v105
	v_cvt_pk_bf16_f32 v25, v66, v125
	v_mov_b32_e32 v112, v128
	v_lshlrev_b32_e32 v64, 16, v24
	v_and_b32_e32 v65, 0xffff0000, v24
	v_and_b32_e32 v102, 0xffff0000, v25
	v_sub_f32_e32 v64, v104, v64
	v_sub_f32_e32 v65, v105, v65
	v_lshlrev_b32_e32 v67, 16, v25
	v_sub_f32_e32 v102, v125, v102
	v_sub_f32_e32 v67, v66, v67
	v_cvt_pk_bf16_f32 v64, v64, v65
	v_cvt_pk_bf16_f32 v65, v67, v102
	v_mov_b32_e32 v102, 0
	v_mov_b32_e32 v67, v232
	v_cvt_pk_fp8_f32 v102, v104, v105
	v_mul_f32_e32 v32, v32, v3
	v_xor_b32_e32 v67, v67, v237
	v_lshl_add_u32 v67, v67, 4, v243
	v_add_u32_e32 v103, 0, v67
	v_cvt_pk_fp8_f32 v102, v66, v125 op_sel:[0,0,1]
	ds_write_b64 v103, v[24:25]
	v_add_u32_e32 v24, s56, v67
	ds_write_b64 v24, v[64:65]
	v_lshl_add_u64 v[24:25], s[24:25], 0, v[252:253]
	v_lshl_add_u64 v[64:65], v[24:25], 0, v[126:127]
	global_store_dword v[64:65], v102, off
	v_mul_f32_e32 v56, v56, v106
	v_ashrrev_i32_e32 v113, 31, v112
	v_lshlrev_b64 v[64:65], 2, v[112:113]
	v_lshl_add_u64 v[102:103], v[64:65], 0, s[40:41]
	v_lshl_add_u64 v[64:65], s[28:29], 0, v[64:65]
	global_load_dwordx4 v[64:67], v[64:65], off offset:1024
	v_lshl_add_u64 v[104:105], v[68:69], 0, v[102:103]
	v_lshl_add_u64 v[108:109], v[116:117], 0, v[102:103]
	global_load_dwordx4 v[102:105], v[104:105], off
	s_nop 0
	global_load_dwordx4 v[108:111], v[108:109], off
	v_mul_f32_e32 v30, v30, v3
	v_mul_f32_e32 v28, v28, v3
	v_mul_f32_e32 v52, v52, v106
	v_mul_f32_e32 v26, v26, v3
	v_mul_f32_e32 v22, v22, v3
	v_mul_f32_e32 v16, v16, v3
	v_mul_f32_e32 v17, v17, v3
	v_mul_f32_e32 v18, v18, v3
	v_mul_f32_e32 v19, v19, v3
	v_mul_f32_e32 v12, v12, v3
	v_mul_f32_e32 v13, v13, v3
	v_mul_f32_e32 v14, v14, v3
	v_mul_f32_e32 v15, v15, v3
	v_mul_f32_e32 v8, v8, v3
	v_mul_f32_e32 v9, v9, v3
	v_mul_f32_e32 v10, v10, v3
	v_mul_f32_e32 v11, v11, v3
	v_mul_f32_e32 v4, v4, v3
	v_mul_f32_e32 v5, v5, v3
	v_mul_f32_e32 v6, v6, v3
	s_mov_b64 s[10:11], 0
	s_waitcnt vmcnt(2)
	v_mul_f32_e32 v60, v60, v64
	v_mul_f32_e32 v34, v34, v64
	s_waitcnt vmcnt(1)
	v_add_f32_e32 v102, 1.0, v102
	s_waitcnt vmcnt(0)
	v_fma_f32 v107, v60, v102, v108
	v_mul_f32_e32 v60, v61, v106
	v_mul_f32_e32 v60, v60, v65
	v_add_f32_e32 v103, 1.0, v103
	v_fma_f32 v114, v60, v103, v109
	v_mul_f32_e32 v60, v62, v106
	v_mul_f32_e32 v60, v60, v66
	v_add_f32_e32 v104, 1.0, v104
	v_fma_f32 v115, v60, v104, v110
	v_mul_f32_e32 v60, v63, v106
	v_mul_f32_e32 v60, v60, v67
	v_add_f32_e32 v105, 1.0, v105
	v_fma_f32 v118, v60, v105, v111
	v_cvt_pk_bf16_f32 v60, v107, v114
	v_cvt_pk_bf16_f32 v61, v115, v118
	v_mul_f32_e32 v32, v32, v66
	v_lshlrev_b32_e32 v62, 16, v60
	v_and_b32_e32 v63, 0xffff0000, v60
	v_and_b32_e32 v120, 0xffff0000, v61
	v_sub_f32_e32 v62, v107, v62
	v_sub_f32_e32 v63, v114, v63
	v_lshlrev_b32_e32 v119, 16, v61
	v_sub_f32_e32 v120, v118, v120
	v_sub_f32_e32 v119, v115, v119
	v_cvt_pk_bf16_f32 v62, v62, v63
	v_cvt_pk_bf16_f32 v63, v119, v120
	v_mov_b32_e32 v120, 0
	v_mov_b32_e32 v119, v232
	v_cvt_pk_fp8_f32 v120, v107, v114
	v_cvt_pk_fp8_f32 v120, v115, v118 op_sel:[0,0,1]
	v_add_u32_e32 v119, 32, v119
	v_xor_b32_e32 v119, v119, v236
	v_lshl_add_u32 v107, v119, 4, v242
	v_add_u32_e32 v114, 0, v107
	ds_write_b64 v114, v[60:61]
	v_add_u32_e32 v60, s56, v107
	ds_write_b64 v60, v[62:63]
	v_lshl_add_u64 v[60:61], v[20:21], 0, v[112:113]
	global_store_dword v[60:61], v120, off offset:256
	v_fma_f32 v60, v34, v102, v108
	v_mul_f32_e32 v34, v35, v3
	v_fma_f32 v62, v32, v104, v110
	v_mul_f32_e32 v32, v33, v3
	v_mul_f32_e32 v34, v34, v65
	v_mul_f32_e32 v32, v32, v67
	v_fma_f32 v61, v34, v103, v109
	v_fmac_f32_e32 v111, v32, v105
	v_cvt_pk_bf16_f32 v32, v60, v61
	v_cvt_pk_bf16_f32 v33, v62, v111
	v_mov_b32_e32 v102, v128
	v_lshlrev_b32_e32 v34, 16, v32
	v_and_b32_e32 v35, 0xffff0000, v32
	v_and_b32_e32 v64, 0xffff0000, v33
	v_sub_f32_e32 v34, v60, v34
	v_sub_f32_e32 v35, v61, v35
	v_lshlrev_b32_e32 v63, 16, v33
	v_sub_f32_e32 v64, v111, v64
	v_sub_f32_e32 v63, v62, v63
	v_cvt_pk_bf16_f32 v34, v34, v35
	v_cvt_pk_bf16_f32 v35, v63, v64
	v_mov_b32_e32 v64, 0
	v_mov_b32_e32 v63, v232
	v_cvt_pk_fp8_f32 v64, v60, v61
	v_mov_b32_e32 v114, v245
	v_add_u32_e32 v63, 32, v63
	v_xor_b32_e32 v63, v63, v237
	v_lshl_add_u32 v60, v63, 4, v243
	v_cvt_pk_fp8_f32 v64, v62, v111 op_sel:[0,0,1]
	v_add_u32_e32 v61, 0, v60
	ds_write_b64 v61, v[32:33]
	v_add_u32_e32 v32, s56, v60
	ds_write_b64 v32, v[34:35]
	v_lshl_add_u64 v[32:33], v[24:25], 0, v[112:113]
	global_store_dword v[32:33], v64, off offset:256
	s_nop 0
	v_ashrrev_i32_e32 v103, 31, v102
	v_lshlrev_b64 v[32:33], 2, v[102:103]
	v_lshl_add_u64 v[60:61], v[32:33], 0, s[42:43]
	v_lshl_add_u64 v[32:33], s[28:29], 0, v[32:33]
	global_load_dwordx4 v[32:35], v[32:33], off offset:2048
	v_lshl_add_u64 v[62:63], v[68:69], 0, v[60:61]
	v_lshl_add_u64 v[64:65], v[116:117], 0, v[60:61]
	global_load_dwordx4 v[60:63], v[62:63], off
	s_nop 0
	global_load_dwordx4 v[64:67], v[64:65], off
	s_waitcnt vmcnt(2)
	v_mul_f32_e32 v56, v56, v32
	v_mul_f32_e32 v30, v30, v32
	s_waitcnt vmcnt(1)
	v_add_f32_e32 v60, 1.0, v60
	s_waitcnt vmcnt(0)
	v_fma_f32 v104, v56, v60, v64
	v_mul_f32_e32 v56, v57, v106
	v_mul_f32_e32 v56, v56, v33
	v_add_f32_e32 v61, 1.0, v61
	v_fma_f32 v105, v56, v61, v65
	v_mul_f32_e32 v56, v58, v106
	v_mul_f32_e32 v56, v56, v34
	v_add_f32_e32 v62, 1.0, v62
	v_fma_f32 v107, v56, v62, v66
	v_mul_f32_e32 v56, v59, v106
	v_mul_f32_e32 v56, v56, v35
	v_add_f32_e32 v63, 1.0, v63
	v_fma_f32 v108, v56, v63, v67
	v_cvt_pk_bf16_f32 v56, v104, v105
	v_cvt_pk_bf16_f32 v57, v107, v108
	v_mul_f32_e32 v28, v28, v34
	v_lshlrev_b32_e32 v58, 16, v56
	v_and_b32_e32 v59, 0xffff0000, v56
	v_and_b32_e32 v110, 0xffff0000, v57
	v_sub_f32_e32 v58, v104, v58
	v_sub_f32_e32 v59, v105, v59
	v_lshlrev_b32_e32 v109, 16, v57
	v_sub_f32_e32 v110, v108, v110
	v_sub_f32_e32 v109, v107, v109
	v_cvt_pk_bf16_f32 v58, v58, v59
	v_cvt_pk_bf16_f32 v59, v109, v110
	v_mov_b32_e32 v110, 0
	v_mov_b32_e32 v109, v232
	v_cvt_pk_fp8_f32 v110, v104, v105
	v_fma_f32 v32, v30, v60, v64
	v_add_u32_e32 v109, 64, v109
	v_xor_b32_e32 v109, v109, v236
	v_lshl_add_u32 v104, v109, 4, v242
	v_cvt_pk_fp8_f32 v110, v107, v108 op_sel:[0,0,1]
	v_add_u32_e32 v105, 0, v104
	ds_write_b64 v105, v[56:57]
	v_add_u32_e32 v56, s56, v104
	v_mul_f32_e32 v30, v31, v3
	v_fma_f32 v34, v28, v62, v66
	v_mul_f32_e32 v28, v29, v3
	ds_write_b64 v56, v[58:59]
	v_lshl_add_u64 v[56:57], v[20:21], 0, v[102:103]
	v_mul_f32_e32 v30, v30, v33
	v_mul_f32_e32 v28, v28, v35
	global_store_dword v[56:57], v110, off offset:512
	v_fma_f32 v33, v30, v61, v65
	v_fmac_f32_e32 v67, v28, v63
	v_cvt_pk_bf16_f32 v28, v32, v33
	v_cvt_pk_bf16_f32 v29, v34, v67
	v_mov_b32_e32 v60, v128
	v_lshlrev_b32_e32 v30, 16, v28
	v_and_b32_e32 v31, 0xffff0000, v28
	v_and_b32_e32 v56, 0xffff0000, v29
	v_sub_f32_e32 v30, v32, v30
	v_sub_f32_e32 v31, v33, v31
	v_lshlrev_b32_e32 v35, 16, v29
	v_sub_f32_e32 v56, v67, v56
	v_sub_f32_e32 v35, v34, v35
	v_cvt_pk_bf16_f32 v30, v30, v31
	v_cvt_pk_bf16_f32 v31, v35, v56
	v_mov_b32_e32 v56, 0
	v_mov_b32_e32 v35, v232
	v_cvt_pk_fp8_f32 v56, v32, v33
	v_cvt_pk_fp8_f32 v56, v34, v67 op_sel:[0,0,1]
	v_add_u32_e32 v35, 64, v35
	v_xor_b32_e32 v35, v35, v237
	v_lshl_add_u32 v32, v35, 4, v243
	v_add_u32_e32 v33, 0, v32
	ds_write_b64 v33, v[28:29]
	v_add_u32_e32 v28, s56, v32
	ds_write_b64 v28, v[30:31]
	v_lshl_add_u64 v[28:29], v[24:25], 0, v[102:103]
	global_store_dword v[28:29], v56, off offset:512
	s_nop 0
	v_ashrrev_i32_e32 v61, 31, v60
	v_lshlrev_b64 v[28:29], 2, v[60:61]
	v_lshl_add_u64 v[32:33], v[28:29], 0, s[44:45]
	v_lshl_add_u64 v[28:29], s[28:29], 0, v[28:29]
	v_lshl_add_u64 v[34:35], v[68:69], 0, v[32:33]
	v_lshl_add_u64 v[56:57], v[116:117], 0, v[32:33]
	global_load_dwordx4 v[28:31], v[28:29], off offset:3072
	s_nop 0
	global_load_dwordx4 v[32:35], v[34:35], off
	s_nop 0
	global_load_dwordx4 v[56:59], v[56:57], off
	s_waitcnt vmcnt(1)
	v_add_f32_e32 v62, 1.0, v32
	v_mul_f32_e32 v32, v53, v106
	v_mul_f32_e32 v32, v32, v29
	v_add_f32_e32 v53, 1.0, v33
	s_waitcnt vmcnt(0)
	v_fma_f32 v63, v32, v53, v57
	v_mul_f32_e32 v32, v54, v106
	v_mul_f32_e32 v32, v32, v30
	v_add_f32_e32 v54, 1.0, v34
	v_fma_f32 v64, v32, v54, v58
	v_mul_f32_e32 v32, v55, v106
	v_mul_f32_e32 v52, v52, v28
	v_mul_f32_e32 v32, v32, v31
	v_add_f32_e32 v55, 1.0, v35
	v_fma_f32 v52, v52, v62, v56
	v_fma_f32 v65, v32, v55, v59
	v_cvt_pk_bf16_f32 v32, v52, v63
	v_cvt_pk_bf16_f32 v33, v64, v65
	v_mul_f32_e32 v26, v26, v28
	v_lshlrev_b32_e32 v34, 16, v32
	v_and_b32_e32 v35, 0xffff0000, v32
	v_and_b32_e32 v67, 0xffff0000, v33
	v_sub_f32_e32 v34, v52, v34
	v_sub_f32_e32 v35, v63, v35
	v_lshlrev_b32_e32 v66, 16, v33
	v_sub_f32_e32 v67, v65, v67
	v_sub_f32_e32 v66, v64, v66
	v_cvt_pk_bf16_f32 v34, v34, v35
	v_cvt_pk_bf16_f32 v35, v66, v67
	v_mov_b32_e32 v67, 0
	v_mov_b32_e32 v66, v232
	v_cvt_pk_fp8_f32 v67, v52, v63
	v_mul_f32_e32 v22, v22, v30
	v_add_u32_e32 v66, 0x60, v66
	v_xor_b32_e32 v66, v66, v236
	v_lshl_add_u32 v52, v66, 4, v242
	v_cvt_pk_fp8_f32 v67, v64, v65 op_sel:[0,0,1]
	v_add_u32_e32 v63, 0, v52
	ds_write_b64 v63, v[32:33]
	v_add_u32_e32 v32, s56, v52
	v_fma_f32 v28, v26, v62, v56
	v_mul_f32_e32 v26, v27, v3
	v_fma_f32 v30, v22, v54, v58
	v_mul_f32_e32 v22, v23, v3
	ds_write_b64 v32, v[34:35]
	v_lshl_add_u64 v[32:33], v[20:21], 0, v[60:61]
	v_mul_f32_e32 v26, v26, v29
	v_mul_f32_e32 v22, v22, v31
	global_store_dword v[32:33], v67, off offset:768
	v_fma_f32 v29, v26, v53, v57
	v_fmac_f32_e32 v59, v22, v55
	v_cvt_pk_bf16_f32 v22, v28, v29
	v_cvt_pk_bf16_f32 v23, v30, v59
	v_mul_f32_e32 v3, v7, v3
	v_lshlrev_b32_e32 v26, 16, v22
	v_and_b32_e32 v27, 0xffff0000, v22
	v_and_b32_e32 v32, 0xffff0000, v23
	v_sub_f32_e32 v26, v28, v26
	v_sub_f32_e32 v27, v29, v27
	v_lshlrev_b32_e32 v31, 16, v23
	v_sub_f32_e32 v32, v59, v32
	v_sub_f32_e32 v31, v30, v31
	v_cvt_pk_bf16_f32 v26, v26, v27
	v_cvt_pk_bf16_f32 v27, v31, v32
	v_mov_b32_e32 v32, 0
	v_mov_b32_e32 v31, v232
	v_cvt_pk_fp8_f32 v32, v28, v29
	v_cvt_pk_fp8_f32 v32, v30, v59 op_sel:[0,0,1]
	v_add_u32_e32 v31, 0x60, v31
	v_xor_b32_e32 v31, v31, v237
	v_lshl_add_u32 v28, v31, 4, v243
	v_add_u32_e32 v29, 0, v28
	ds_write_b64 v29, v[22:23]
	v_add_u32_e32 v22, s56, v28
	ds_write_b64 v22, v[26:27]
	v_lshl_add_u64 v[22:23], v[24:25], 0, v[60:61]
	global_store_dword v[22:23], v32, off offset:768
	v_mov_b32_e32 v22, v128
	v_mov_b32_e32 v59, 0
	v_ashrrev_i32_e32 v23, 31, v22
	v_lshl_add_u64 v[30:31], v[22:23], 2, v[152:153]
	v_lshl_add_u64 v[26:27], s[28:29], 0, v[30:31]
	global_load_dwordx4 v[26:29], v[26:27], off
	v_lshl_add_u64 v[32:33], v[68:69], 0, v[30:31]
	v_lshl_add_u64 v[34:35], v[116:117], 0, v[30:31]
	global_load_dwordx4 v[30:33], v[32:33], off
	s_nop 0
	global_load_dwordx4 v[54:57], v[34:35], off
	v_mul_f32_e32 v34, v48, v106
	v_mul_f32_e32 v48, v51, v106
	v_mov_b32_e32 v60, 0
	s_waitcnt vmcnt(2)
	v_mul_f32_e32 v34, v34, v26
	v_mul_f32_e32 v48, v48, v29
	s_waitcnt vmcnt(1)
	v_add_f32_e32 v35, 1.0, v30
	s_waitcnt vmcnt(0)
	v_fma_f32 v30, v34, v35, v54
	v_mul_f32_e32 v34, v49, v106
	v_mul_f32_e32 v34, v34, v27
	v_add_f32_e32 v58, 1.0, v31
	v_fma_f32 v31, v34, v58, v55
	v_cvt_pk_fp8_f32 v59, v30, v31
	v_mul_f32_e32 v34, v50, v106
	v_mul_f32_e32 v34, v34, v28
	v_add_f32_e32 v32, 1.0, v32
	v_add_f32_e32 v33, 1.0, v33
	v_mul_f32_e32 v16, v16, v26
	v_mul_f32_e32 v17, v17, v27
	v_fma_f32 v34, v34, v32, v56
	v_fma_f32 v50, v48, v33, v57
	v_fma_f32 v16, v16, v35, v54
	v_fma_f32 v17, v17, v58, v55
	v_mul_f32_e32 v18, v18, v28
	v_mov_b32_e32 v28, 0
	v_cvt_pk_bf16_f32 v48, v30, v31
	v_cvt_pk_fp8_f32 v59, v34, v50 op_sel:[0,0,1]
	v_and_b32_e32 v52, 0xffff0000, v48
	v_cvt_pk_fp8_f32 v28, v16, v17
	v_cvt_pk_bf16_f32 v49, v34, v50
	v_lshlrev_b32_e32 v51, 16, v48
	v_sub_f32_e32 v52, v31, v52
	v_lshlrev_b32_e32 v53, 16, v49
	v_and_b32_e32 v31, 0xffff0000, v49
	v_sub_f32_e32 v51, v30, v51
	v_sub_f32_e32 v30, v34, v53
	v_sub_f32_e32 v31, v50, v31
	v_mul_f32_e32 v19, v19, v29
	v_cvt_pk_bf16_f32 v52, v51, v52
	v_cvt_pk_bf16_f32 v53, v30, v31
	v_lshl_add_u64 v[30:31], v[20:21], 0, v[22:23]
	v_fma_f32 v18, v18, v32, v56
	v_fmac_f32_e32 v57, v19, v33
	global_store_dword v[30:31], v59, off offset:1024
	v_cvt_pk_bf16_f32 v50, v16, v17
	v_cvt_pk_fp8_f32 v28, v18, v57 op_sel:[0,0,1]
	v_and_b32_e32 v26, 0xffff0000, v50
	v_cvt_pk_bf16_f32 v51, v18, v57
	v_lshlrev_b32_e32 v19, 16, v50
	v_sub_f32_e32 v26, v17, v26
	v_lshlrev_b32_e32 v27, 16, v51
	v_and_b32_e32 v17, 0xffff0000, v51
	v_sub_f32_e32 v19, v16, v19
	v_sub_f32_e32 v16, v18, v27
	v_sub_f32_e32 v17, v57, v17
	v_cvt_pk_bf16_f32 v54, v19, v26
	v_cvt_pk_bf16_f32 v55, v16, v17
	v_lshl_add_u64 v[16:17], v[24:25], 0, v[22:23]
	v_mov_b32_e32 v22, v128
	global_store_dword v[16:17], v28, off offset:1024
	v_mul_f32_e32 v34, v44, v106
	v_ashrrev_i32_e32 v23, 31, v22
	v_lshl_add_u64 v[26:27], v[22:23], 2, v[144:145]
	v_lshl_add_u64 v[16:17], s[28:29], 0, v[26:27]
	global_load_dwordx4 v[16:19], v[16:17], off
	v_lshl_add_u64 v[28:29], v[68:69], 0, v[26:27]
	v_lshl_add_u64 v[30:31], v[116:117], 0, v[26:27]
	global_load_dwordx4 v[26:29], v[28:29], off
	s_nop 0
	global_load_dwordx4 v[30:33], v[30:31], off
	s_waitcnt vmcnt(2)
	v_mul_f32_e32 v34, v34, v16
	v_mul_f32_e32 v12, v12, v16
	s_waitcnt vmcnt(1)
	v_add_f32_e32 v35, 1.0, v26
	s_waitcnt vmcnt(0)
	v_fma_f32 v26, v34, v35, v30
	v_mul_f32_e32 v34, v45, v106
	v_mul_f32_e32 v34, v34, v17
	v_add_f32_e32 v44, 1.0, v27
	v_fma_f32 v27, v34, v44, v31
	v_cvt_pk_fp8_f32 v60, v26, v27
	v_mul_f32_e32 v34, v46, v106
	v_mul_f32_e32 v45, v47, v106
	v_mul_f32_e32 v34, v34, v18
	v_add_f32_e32 v28, 1.0, v28
	v_mul_f32_e32 v45, v45, v19
	v_add_f32_e32 v29, 1.0, v29
	v_mul_f32_e32 v13, v13, v17
	v_fma_f32 v34, v34, v28, v32
	v_fma_f32 v45, v45, v29, v33
	v_fma_f32 v12, v12, v35, v30
	v_fma_f32 v13, v13, v44, v31
	v_mul_f32_e32 v14, v14, v18
	v_mov_b32_e32 v18, 0
	v_cvt_pk_bf16_f32 v46, v26, v27
	v_cvt_pk_fp8_f32 v60, v34, v45 op_sel:[0,0,1]
	v_and_b32_e32 v57, 0xffff0000, v46
	v_cvt_pk_fp8_f32 v18, v12, v13
	v_cvt_pk_bf16_f32 v47, v34, v45
	v_lshlrev_b32_e32 v56, 16, v46
	v_sub_f32_e32 v57, v27, v57
	v_lshlrev_b32_e32 v58, 16, v47
	v_and_b32_e32 v27, 0xffff0000, v47
	v_sub_f32_e32 v56, v26, v56
	v_sub_f32_e32 v26, v34, v58
	v_sub_f32_e32 v27, v45, v27
	v_mul_f32_e32 v15, v15, v19
	v_cvt_pk_bf16_f32 v58, v56, v57
	v_cvt_pk_bf16_f32 v59, v26, v27
	v_lshl_add_u64 v[26:27], v[20:21], 0, v[22:23]
	v_fma_f32 v14, v14, v28, v32
	v_fmac_f32_e32 v33, v15, v29
	global_store_dword v[26:27], v60, off offset:1280
	v_cvt_pk_bf16_f32 v56, v12, v13
	v_cvt_pk_fp8_f32 v18, v14, v33 op_sel:[0,0,1]
	v_and_b32_e32 v16, 0xffff0000, v56
	v_cvt_pk_bf16_f32 v57, v14, v33
	v_lshlrev_b32_e32 v15, 16, v56
	v_sub_f32_e32 v16, v13, v16
	v_lshlrev_b32_e32 v17, 16, v57
	v_and_b32_e32 v13, 0xffff0000, v57
	v_sub_f32_e32 v15, v12, v15
	v_sub_f32_e32 v12, v14, v17
	v_sub_f32_e32 v13, v33, v13
	v_cvt_pk_bf16_f32 v60, v15, v16
	v_cvt_pk_bf16_f32 v61, v12, v13
	v_lshl_add_u64 v[12:13], v[24:25], 0, v[22:23]
	v_mov_b32_e32 v22, v128
	global_store_dword v[12:13], v18, off offset:1280
	v_mul_f32_e32 v30, v40, v106
	v_ashrrev_i32_e32 v23, 31, v22
	v_lshl_add_u64 v[16:17], v[22:23], 2, v[146:147]
	v_lshl_add_u64 v[12:13], s[28:29], 0, v[16:17]
	global_load_dwordx4 v[12:15], v[12:13], off
	v_lshl_add_u64 v[18:19], v[68:69], 0, v[16:17]
	v_lshl_add_u64 v[26:27], v[116:117], 0, v[16:17]
	global_load_dwordx4 v[16:19], v[18:19], off
	s_nop 0
	global_load_dwordx4 v[26:29], v[26:27], off
	v_mul_f32_e32 v33, v43, v106
	s_waitcnt vmcnt(2)
	v_mul_f32_e32 v30, v30, v12
	v_mul_f32_e32 v33, v33, v15
	s_waitcnt vmcnt(1)
	v_add_f32_e32 v31, 1.0, v16
	s_waitcnt vmcnt(0)
	v_fma_f32 v16, v30, v31, v26
	v_mul_f32_e32 v30, v41, v106
	v_mul_f32_e32 v30, v30, v13
	v_add_f32_e32 v32, 1.0, v17
	v_fma_f32 v17, v30, v32, v27
	v_mov_b32_e32 v41, 0
	v_cvt_pk_fp8_f32 v41, v16, v17
	v_mul_f32_e32 v30, v42, v106
	v_mul_f32_e32 v30, v30, v14
	v_add_f32_e32 v18, 1.0, v18
	v_add_f32_e32 v19, 1.0, v19
	v_mul_f32_e32 v8, v8, v12
	v_mul_f32_e32 v9, v9, v13
	v_fma_f32 v30, v30, v18, v28
	v_fma_f32 v33, v33, v19, v29
	v_fma_f32 v8, v8, v31, v26
	v_fma_f32 v9, v9, v32, v27
	v_mul_f32_e32 v10, v10, v14
	v_mov_b32_e32 v14, 0
	v_cvt_pk_bf16_f32 v62, v16, v17
	v_cvt_pk_fp8_f32 v41, v30, v33 op_sel:[0,0,1]
	v_and_b32_e32 v35, 0xffff0000, v62
	v_cvt_pk_fp8_f32 v14, v8, v9
	v_cvt_pk_bf16_f32 v63, v30, v33
	v_lshlrev_b32_e32 v34, 16, v62
	v_sub_f32_e32 v35, v17, v35
	v_lshlrev_b32_e32 v40, 16, v63
	v_and_b32_e32 v17, 0xffff0000, v63
	v_sub_f32_e32 v34, v16, v34
	v_sub_f32_e32 v16, v30, v40
	v_sub_f32_e32 v17, v33, v17
	v_mul_f32_e32 v11, v11, v15
	v_cvt_pk_bf16_f32 v66, v34, v35
	v_cvt_pk_bf16_f32 v67, v16, v17
	v_lshl_add_u64 v[16:17], v[20:21], 0, v[22:23]
	v_fma_f32 v10, v10, v18, v28
	v_fmac_f32_e32 v29, v11, v19
	global_store_dword v[16:17], v41, off offset:1536
	v_cvt_pk_bf16_f32 v64, v8, v9
	v_cvt_pk_fp8_f32 v14, v10, v29 op_sel:[0,0,1]
	v_and_b32_e32 v12, 0xffff0000, v64
	v_cvt_pk_bf16_f32 v65, v10, v29
	v_lshlrev_b32_e32 v11, 16, v64
	v_sub_f32_e32 v12, v9, v12
	v_lshlrev_b32_e32 v13, 16, v65
	v_and_b32_e32 v9, 0xffff0000, v65
	v_sub_f32_e32 v11, v8, v11
	v_sub_f32_e32 v8, v10, v13
	v_sub_f32_e32 v9, v29, v9
	v_cvt_pk_bf16_f32 v102, v11, v12
	v_cvt_pk_bf16_f32 v103, v8, v9
	v_lshl_add_u64 v[8:9], v[24:25], 0, v[22:23]
	v_mov_b32_e32 v22, v128
	global_store_dword v[8:9], v14, off offset:1536
	v_mul_f32_e32 v26, v36, v106
	v_ashrrev_i32_e32 v23, 31, v22
	v_lshl_add_u64 v[12:13], v[22:23], 2, v[148:149]
	v_lshl_add_u64 v[8:9], s[28:29], 0, v[12:13]
	global_load_dwordx4 v[8:11], v[8:9], off
	v_lshl_add_u64 v[14:15], v[68:69], 0, v[12:13]
	v_lshl_add_u64 v[16:17], v[116:117], 0, v[12:13]
	global_load_dwordx4 v[12:15], v[14:15], off
	s_nop 0
	global_load_dwordx4 v[16:19], v[16:17], off
	v_mov_b32_e32 v33, 0
	v_mul_f32_e32 v29, v39, v106
	s_waitcnt vmcnt(2)
	v_mul_f32_e32 v26, v26, v8
	v_mul_f32_e32 v29, v29, v11
	s_waitcnt vmcnt(1)
	v_add_f32_e32 v27, 1.0, v12
	s_waitcnt vmcnt(0)
	v_fma_f32 v12, v26, v27, v16
	v_mul_f32_e32 v26, v37, v106
	v_mul_f32_e32 v26, v26, v9
	v_add_f32_e32 v28, 1.0, v13
	v_fma_f32 v13, v26, v28, v17
	v_cvt_pk_fp8_f32 v33, v12, v13
	v_mul_f32_e32 v26, v38, v106
	v_mul_f32_e32 v26, v26, v10
	v_add_f32_e32 v14, 1.0, v14
	v_add_f32_e32 v15, 1.0, v15
	v_mul_f32_e32 v4, v4, v8
	v_mul_f32_e32 v5, v5, v9
	v_fma_f32 v26, v26, v14, v18
	v_fma_f32 v29, v29, v15, v19
	v_fma_f32 v4, v4, v27, v16
	v_fma_f32 v5, v5, v28, v17
	v_mov_b32_e32 v9, 0
	v_cvt_pk_bf16_f32 v68, v12, v13
	v_cvt_pk_fp8_f32 v33, v26, v29 op_sel:[0,0,1]
	v_and_b32_e32 v31, 0xffff0000, v68
	v_cvt_pk_fp8_f32 v9, v4, v5
	v_cvt_pk_bf16_f32 v69, v26, v29
	v_lshlrev_b32_e32 v30, 16, v68
	v_sub_f32_e32 v31, v13, v31
	v_lshlrev_b32_e32 v32, 16, v69
	v_and_b32_e32 v13, 0xffff0000, v69
	v_sub_f32_e32 v30, v12, v30
	v_sub_f32_e32 v12, v26, v32
	v_sub_f32_e32 v13, v29, v13
	v_mul_f32_e32 v6, v6, v10
	v_mul_f32_e32 v3, v3, v11
	v_cvt_pk_bf16_f32 v106, v30, v31
	v_cvt_pk_bf16_f32 v107, v12, v13
	v_lshl_add_u64 v[12:13], v[20:21], 0, v[22:23]
	v_fma_f32 v6, v6, v14, v18
	v_fmac_f32_e32 v19, v3, v15
	global_store_dword v[12:13], v33, off offset:1792
	v_cvt_pk_bf16_f32 v104, v4, v5
	v_cvt_pk_fp8_f32 v9, v6, v19 op_sel:[0,0,1]
	v_and_b32_e32 v7, 0xffff0000, v104
	v_cvt_pk_bf16_f32 v105, v6, v19
	v_lshlrev_b32_e32 v3, 16, v104
	v_sub_f32_e32 v7, v5, v7
	v_lshlrev_b32_e32 v8, 16, v105
	v_and_b32_e32 v5, 0xffff0000, v105
	v_sub_f32_e32 v3, v4, v3
	v_sub_f32_e32 v4, v6, v8
	v_sub_f32_e32 v5, v19, v5
	v_cvt_pk_bf16_f32 v108, v3, v7
	v_cvt_pk_bf16_f32 v109, v4, v5
	v_lshl_add_u64 v[4:5], v[24:25], 0, v[22:23]
	global_store_dword v[4:5], v9, off offset:1792
	v_mov_b32_e32 v4, v2
	v_mov_b32_e32 v5, v2
	v_mov_b32_e32 v3, v2
	v_mov_b64_e32 v[8:9], v[4:5]
	v_mov_b64_e32 v[12:13], v[4:5]
	v_mov_b64_e32 v[16:17], v[4:5]
	v_mov_b64_e32 v[20:21], v[4:5]
	v_mov_b64_e32 v[24:25], v[4:5]
	v_mov_b64_e32 v[28:29], v[4:5]
	v_mov_b64_e32 v[6:7], v[2:3]
	v_mov_b64_e32 v[10:11], v[2:3]
	v_mov_b64_e32 v[14:15], v[2:3]
	v_mov_b64_e32 v[18:19], v[2:3]
	v_mov_b64_e32 v[22:23], v[2:3]
	v_mov_b64_e32 v[26:27], v[2:3]
	v_subrev_u32_e32 v222, s76, v136
	s_add_u32 s98, s76, 0x38178000
	s_addc_u32 s99, s77, 0
	s_add_u32 s100, s76, 0x381c8000
	s_addc_u32 s101, s77, 0
	v_add_u32_e32 v223, 0x10000, v222
	v_add_u32_e32 v224, 0x20000, v222
	global_load_dwordx4 v[150:153], v222, s[98:99] offset:0
	global_load_dwordx4 v[154:157], v222, s[100:101] offset:0
	global_load_dwordx4 v[158:161], v223, s[98:99] offset:0
	global_load_dwordx4 v[162:165], v223, s[100:101] offset:0
	global_load_dwordx4 v[166:169], v224, s[98:99] offset:0
	global_load_dwordx4 v[170:173], v224, s[100:101] offset:0
	global_load_dwordx4 v[174:177], v222, s[98:99] offset:64
	global_load_dwordx4 v[178:181], v222, s[100:101] offset:64
	global_load_dwordx4 v[182:185], v223, s[98:99] offset:64
	global_load_dwordx4 v[186:189], v223, s[100:101] offset:64
	global_load_dwordx4 v[190:193], v224, s[98:99] offset:64
	global_load_dwordx4 v[194:197], v224, s[100:101] offset:64
	s_waitcnt lgkmcnt(0)
	s_barrier
	v_mov_b32_e32 v3, v245
	v_xor_b32_e32 v4, v3, v1
	v_xor_b32_e32 v3, v3, v238
	v_lshl_add_u32 v4, v4, 4, v233
	v_lshl_add_u32 v3, v3, 4, v239
	v_add_u32_e32 v5, s56, v4
	v_add_u32_e32 v115, s56, v3
	ds_read_b128 v[34:37], v4
	ds_read_b128 v[30:33], v5
	ds_read_b128 v[42:45], v3
	ds_read_b128 v[38:41], v115
	global_load_dwordx4 v[198:201], v222, s[98:99] offset:128
	global_load_dwordx4 v[202:205], v222, s[100:101] offset:128
	global_load_dwordx4 v[206:209], v223, s[98:99] offset:128
	global_load_dwordx4 v[210:213], v223, s[100:101] offset:128
	global_load_dwordx4 v[214:217], v224, s[98:99] offset:128
	global_load_dwordx4 v[218:221], v224, s[100:101] offset:128
	v_add_u32_e32 v3, 4, v245
	v_xor_b32_e32 v4, v3, v1
	v_xor_b32_e32 v3, v3, v238
	v_lshl_add_u32 v4, v4, 4, v233
	v_lshl_add_u32 v3, v3, 4, v239
	v_add_u32_e32 v5, s56, v4
	v_add_u32_e32 v115, s56, v3
	ds_read_b128 v[110:113], v4
	ds_read_b128 v[116:119], v5
	ds_read_b128 v[120:123], v3
	ds_read_b128 v[124:127], v115
	s_waitcnt vmcnt(12) lgkmcnt(4)
	v_mfma_f32_16x16x32_bf16 v[26:29], v[150:153], v[34:37], v[26:29]
	v_mfma_f32_16x16x32_bf16 v[14:17], v[150:153], v[42:45], v[14:17]
	v_mfma_f32_16x16x32_bf16 v[26:29], v[154:157], v[34:37], v[26:29]
	v_mfma_f32_16x16x32_bf16 v[14:17], v[154:157], v[42:45], v[14:17]
	v_mfma_f32_16x16x32_bf16 v[26:29], v[150:153], v[30:33], v[26:29]
	v_mfma_f32_16x16x32_bf16 v[14:17], v[150:153], v[38:41], v[14:17]
	v_mfma_f32_16x16x32_bf16 v[22:25], v[158:161], v[34:37], v[22:25]
	v_mfma_f32_16x16x32_bf16 v[10:13], v[158:161], v[42:45], v[10:13]
	v_mfma_f32_16x16x32_bf16 v[22:25], v[162:165], v[34:37], v[22:25]
	v_mfma_f32_16x16x32_bf16 v[10:13], v[162:165], v[42:45], v[10:13]
	v_mfma_f32_16x16x32_bf16 v[22:25], v[158:161], v[30:33], v[22:25]
	v_mfma_f32_16x16x32_bf16 v[10:13], v[158:161], v[38:41], v[10:13]
	s_and_b64 vcc, exec, s[8:9]
	s_cbranch_vccz .Lrg_skip_0
	v_mfma_f32_16x16x32_bf16 v[18:21], v[166:169], v[34:37], v[18:21]
	v_mfma_f32_16x16x32_bf16 v[6:9], v[166:169], v[42:45], v[6:9]
	v_mfma_f32_16x16x32_bf16 v[18:21], v[170:173], v[34:37], v[18:21]
	v_mfma_f32_16x16x32_bf16 v[6:9], v[170:173], v[42:45], v[6:9]
	v_mfma_f32_16x16x32_bf16 v[18:21], v[166:169], v[30:33], v[18:21]
	v_mfma_f32_16x16x32_bf16 v[6:9], v[166:169], v[38:41], v[6:9]
.Lrg_skip_0:
	global_load_dwordx4 v[150:153], v222, s[98:99] offset:192
	global_load_dwordx4 v[154:157], v222, s[100:101] offset:192
	global_load_dwordx4 v[158:161], v223, s[98:99] offset:192
	global_load_dwordx4 v[162:165], v223, s[100:101] offset:192
	global_load_dwordx4 v[166:169], v224, s[98:99] offset:192
	global_load_dwordx4 v[170:173], v224, s[100:101] offset:192
	v_add_u32_e32 v3, 8, v245
	v_xor_b32_e32 v4, v3, v1
	v_xor_b32_e32 v3, v3, v238
	v_lshl_add_u32 v4, v4, 4, v233
	v_lshl_add_u32 v3, v3, 4, v239
	v_add_u32_e32 v5, s56, v4
	v_add_u32_e32 v115, s56, v3
	ds_read_b128 v[34:37], v4
	ds_read_b128 v[30:33], v5
	ds_read_b128 v[42:45], v3
	ds_read_b128 v[38:41], v115
	s_waitcnt vmcnt(12) lgkmcnt(4)
	v_mfma_f32_16x16x32_bf16 v[26:29], v[174:177], v[110:113], v[26:29]
	v_mfma_f32_16x16x32_bf16 v[14:17], v[174:177], v[120:123], v[14:17]
	v_mfma_f32_16x16x32_bf16 v[26:29], v[178:181], v[110:113], v[26:29]
	v_mfma_f32_16x16x32_bf16 v[14:17], v[178:181], v[120:123], v[14:17]
	v_mfma_f32_16x16x32_bf16 v[26:29], v[174:177], v[116:119], v[26:29]
	v_mfma_f32_16x16x32_bf16 v[14:17], v[174:177], v[124:127], v[14:17]
	v_mfma_f32_16x16x32_bf16 v[22:25], v[182:185], v[110:113], v[22:25]
	v_mfma_f32_16x16x32_bf16 v[10:13], v[182:185], v[120:123], v[10:13]
	v_mfma_f32_16x16x32_bf16 v[22:25], v[186:189], v[110:113], v[22:25]
	v_mfma_f32_16x16x32_bf16 v[10:13], v[186:189], v[120:123], v[10:13]
	v_mfma_f32_16x16x32_bf16 v[22:25], v[182:185], v[116:119], v[22:25]
	v_mfma_f32_16x16x32_bf16 v[10:13], v[182:185], v[124:127], v[10:13]
	s_and_b64 vcc, exec, s[8:9]
	s_cbranch_vccz .Lrg_skip_1
	v_mfma_f32_16x16x32_bf16 v[18:21], v[190:193], v[110:113], v[18:21]
	v_mfma_f32_16x16x32_bf16 v[6:9], v[190:193], v[120:123], v[6:9]
	v_mfma_f32_16x16x32_bf16 v[18:21], v[194:197], v[110:113], v[18:21]
	v_mfma_f32_16x16x32_bf16 v[6:9], v[194:197], v[120:123], v[6:9]
	v_mfma_f32_16x16x32_bf16 v[18:21], v[190:193], v[116:119], v[18:21]
	v_mfma_f32_16x16x32_bf16 v[6:9], v[190:193], v[124:127], v[6:9]
.Lrg_skip_1:
	global_load_dwordx4 v[174:177], v222, s[98:99] offset:256
	global_load_dwordx4 v[178:181], v222, s[100:101] offset:256
	global_load_dwordx4 v[182:185], v223, s[98:99] offset:256
	global_load_dwordx4 v[186:189], v223, s[100:101] offset:256
	global_load_dwordx4 v[190:193], v224, s[98:99] offset:256
	global_load_dwordx4 v[194:197], v224, s[100:101] offset:256
	v_add_u32_e32 v3, 12, v245
	v_xor_b32_e32 v4, v3, v1
	v_xor_b32_e32 v3, v3, v238
	v_lshl_add_u32 v4, v4, 4, v233
	v_lshl_add_u32 v3, v3, 4, v239
	v_add_u32_e32 v5, s56, v4
	v_add_u32_e32 v115, s56, v3
	ds_read_b128 v[110:113], v4
	ds_read_b128 v[116:119], v5
	ds_read_b128 v[120:123], v3
	ds_read_b128 v[124:127], v115
	s_waitcnt vmcnt(12) lgkmcnt(4)
	v_mfma_f32_16x16x32_bf16 v[26:29], v[198:201], v[34:37], v[26:29]
	v_mfma_f32_16x16x32_bf16 v[14:17], v[198:201], v[42:45], v[14:17]
	v_mfma_f32_16x16x32_bf16 v[26:29], v[202:205], v[34:37], v[26:29]
	v_mfma_f32_16x16x32_bf16 v[14:17], v[202:205], v[42:45], v[14:17]
	v_mfma_f32_16x16x32_bf16 v[26:29], v[198:201], v[30:33], v[26:29]
	v_mfma_f32_16x16x32_bf16 v[14:17], v[198:201], v[38:41], v[14:17]
	v_mfma_f32_16x16x32_bf16 v[22:25], v[206:209], v[34:37], v[22:25]
	v_mfma_f32_16x16x32_bf16 v[10:13], v[206:209], v[42:45], v[10:13]
	v_mfma_f32_16x16x32_bf16 v[22:25], v[210:213], v[34:37], v[22:25]
	v_mfma_f32_16x16x32_bf16 v[10:13], v[210:213], v[42:45], v[10:13]
	v_mfma_f32_16x16x32_bf16 v[22:25], v[206:209], v[30:33], v[22:25]
	v_mfma_f32_16x16x32_bf16 v[10:13], v[206:209], v[38:41], v[10:13]
	s_and_b64 vcc, exec, s[8:9]
	s_cbranch_vccz .Lrg_skip_2
	v_mfma_f32_16x16x32_bf16 v[18:21], v[214:217], v[34:37], v[18:21]
	v_mfma_f32_16x16x32_bf16 v[6:9], v[214:217], v[42:45], v[6:9]
	v_mfma_f32_16x16x32_bf16 v[18:21], v[218:221], v[34:37], v[18:21]
	v_mfma_f32_16x16x32_bf16 v[6:9], v[218:221], v[42:45], v[6:9]
	v_mfma_f32_16x16x32_bf16 v[18:21], v[214:217], v[30:33], v[18:21]
	v_mfma_f32_16x16x32_bf16 v[6:9], v[214:217], v[38:41], v[6:9]
.Lrg_skip_2:
	global_load_dwordx4 v[198:201], v222, s[98:99] offset:320
	global_load_dwordx4 v[202:205], v222, s[100:101] offset:320
	global_load_dwordx4 v[206:209], v223, s[98:99] offset:320
	global_load_dwordx4 v[210:213], v223, s[100:101] offset:320
	global_load_dwordx4 v[214:217], v224, s[98:99] offset:320
	global_load_dwordx4 v[218:221], v224, s[100:101] offset:320
	v_add_u32_e32 v3, 16, v245
	v_xor_b32_e32 v4, v3, v1
	v_xor_b32_e32 v3, v3, v238
	v_lshl_add_u32 v4, v4, 4, v233
	v_lshl_add_u32 v3, v3, 4, v239
	v_add_u32_e32 v5, s56, v4
	v_add_u32_e32 v115, s56, v3
	ds_read_b128 v[34:37], v4
	ds_read_b128 v[30:33], v5
	ds_read_b128 v[42:45], v3
	ds_read_b128 v[38:41], v115
	s_waitcnt vmcnt(12) lgkmcnt(4)
	v_mfma_f32_16x16x32_bf16 v[26:29], v[150:153], v[110:113], v[26:29]
	v_mfma_f32_16x16x32_bf16 v[14:17], v[150:153], v[120:123], v[14:17]
	v_mfma_f32_16x16x32_bf16 v[26:29], v[154:157], v[110:113], v[26:29]
	v_mfma_f32_16x16x32_bf16 v[14:17], v[154:157], v[120:123], v[14:17]
	v_mfma_f32_16x16x32_bf16 v[26:29], v[150:153], v[116:119], v[26:29]
	v_mfma_f32_16x16x32_bf16 v[14:17], v[150:153], v[124:127], v[14:17]
	v_mfma_f32_16x16x32_bf16 v[22:25], v[158:161], v[110:113], v[22:25]
	v_mfma_f32_16x16x32_bf16 v[10:13], v[158:161], v[120:123], v[10:13]
	v_mfma_f32_16x16x32_bf16 v[22:25], v[162:165], v[110:113], v[22:25]
	v_mfma_f32_16x16x32_bf16 v[10:13], v[162:165], v[120:123], v[10:13]
	v_mfma_f32_16x16x32_bf16 v[22:25], v[158:161], v[116:119], v[22:25]
	v_mfma_f32_16x16x32_bf16 v[10:13], v[158:161], v[124:127], v[10:13]
	s_and_b64 vcc, exec, s[8:9]
	s_cbranch_vccz .Lrg_skip_3
	v_mfma_f32_16x16x32_bf16 v[18:21], v[166:169], v[110:113], v[18:21]
	v_mfma_f32_16x16x32_bf16 v[6:9], v[166:169], v[120:123], v[6:9]
	v_mfma_f32_16x16x32_bf16 v[18:21], v[170:173], v[110:113], v[18:21]
	v_mfma_f32_16x16x32_bf16 v[6:9], v[170:173], v[120:123], v[6:9]
	v_mfma_f32_16x16x32_bf16 v[18:21], v[166:169], v[116:119], v[18:21]
	v_mfma_f32_16x16x32_bf16 v[6:9], v[166:169], v[124:127], v[6:9]
.Lrg_skip_3:
	global_load_dwordx4 v[150:153], v222, s[98:99] offset:384
	global_load_dwordx4 v[154:157], v222, s[100:101] offset:384
	global_load_dwordx4 v[158:161], v223, s[98:99] offset:384
	global_load_dwordx4 v[162:165], v223, s[100:101] offset:384
	global_load_dwordx4 v[166:169], v224, s[98:99] offset:384
	global_load_dwordx4 v[170:173], v224, s[100:101] offset:384
	v_add_u32_e32 v3, 20, v245
	v_xor_b32_e32 v4, v3, v1
	v_xor_b32_e32 v3, v3, v238
	v_lshl_add_u32 v4, v4, 4, v233
	v_lshl_add_u32 v3, v3, 4, v239
	v_add_u32_e32 v5, s56, v4
	v_add_u32_e32 v115, s56, v3
	ds_read_b128 v[110:113], v4
	ds_read_b128 v[116:119], v5
	ds_read_b128 v[120:123], v3
	ds_read_b128 v[124:127], v115
	s_waitcnt vmcnt(12) lgkmcnt(4)
	v_mfma_f32_16x16x32_bf16 v[26:29], v[174:177], v[34:37], v[26:29]
	v_mfma_f32_16x16x32_bf16 v[14:17], v[174:177], v[42:45], v[14:17]
	v_mfma_f32_16x16x32_bf16 v[26:29], v[178:181], v[34:37], v[26:29]
	v_mfma_f32_16x16x32_bf16 v[14:17], v[178:181], v[42:45], v[14:17]
	v_mfma_f32_16x16x32_bf16 v[26:29], v[174:177], v[30:33], v[26:29]
	v_mfma_f32_16x16x32_bf16 v[14:17], v[174:177], v[38:41], v[14:17]
	v_mfma_f32_16x16x32_bf16 v[22:25], v[182:185], v[34:37], v[22:25]
	v_mfma_f32_16x16x32_bf16 v[10:13], v[182:185], v[42:45], v[10:13]
	v_mfma_f32_16x16x32_bf16 v[22:25], v[186:189], v[34:37], v[22:25]
	v_mfma_f32_16x16x32_bf16 v[10:13], v[186:189], v[42:45], v[10:13]
	v_mfma_f32_16x16x32_bf16 v[22:25], v[182:185], v[30:33], v[22:25]
	v_mfma_f32_16x16x32_bf16 v[10:13], v[182:185], v[38:41], v[10:13]
	s_and_b64 vcc, exec, s[8:9]
	s_cbranch_vccz .Lrg_skip_4
	v_mfma_f32_16x16x32_bf16 v[18:21], v[190:193], v[34:37], v[18:21]
	v_mfma_f32_16x16x32_bf16 v[6:9], v[190:193], v[42:45], v[6:9]
	v_mfma_f32_16x16x32_bf16 v[18:21], v[194:197], v[34:37], v[18:21]
	v_mfma_f32_16x16x32_bf16 v[6:9], v[194:197], v[42:45], v[6:9]
	v_mfma_f32_16x16x32_bf16 v[18:21], v[190:193], v[30:33], v[18:21]
	v_mfma_f32_16x16x32_bf16 v[6:9], v[190:193], v[38:41], v[6:9]
.Lrg_skip_4:
	global_load_dwordx4 v[174:177], v222, s[98:99] offset:448
	global_load_dwordx4 v[178:181], v222, s[100:101] offset:448
	global_load_dwordx4 v[182:185], v223, s[98:99] offset:448
	global_load_dwordx4 v[186:189], v223, s[100:101] offset:448
	global_load_dwordx4 v[190:193], v224, s[98:99] offset:448
	global_load_dwordx4 v[194:197], v224, s[100:101] offset:448
	v_add_u32_e32 v3, 24, v245
	v_xor_b32_e32 v4, v3, v1
	v_xor_b32_e32 v3, v3, v238
	v_lshl_add_u32 v4, v4, 4, v233
	v_lshl_add_u32 v3, v3, 4, v239
	v_add_u32_e32 v5, s56, v4
	v_add_u32_e32 v115, s56, v3
	ds_read_b128 v[34:37], v4
	ds_read_b128 v[30:33], v5
	ds_read_b128 v[42:45], v3
	ds_read_b128 v[38:41], v115
	s_waitcnt vmcnt(12) lgkmcnt(4)
	v_mfma_f32_16x16x32_bf16 v[26:29], v[198:201], v[110:113], v[26:29]
	v_mfma_f32_16x16x32_bf16 v[14:17], v[198:201], v[120:123], v[14:17]
	v_mfma_f32_16x16x32_bf16 v[26:29], v[202:205], v[110:113], v[26:29]
	v_mfma_f32_16x16x32_bf16 v[14:17], v[202:205], v[120:123], v[14:17]
	v_mfma_f32_16x16x32_bf16 v[26:29], v[198:201], v[116:119], v[26:29]
	v_mfma_f32_16x16x32_bf16 v[14:17], v[198:201], v[124:127], v[14:17]
	v_mfma_f32_16x16x32_bf16 v[22:25], v[206:209], v[110:113], v[22:25]
	v_mfma_f32_16x16x32_bf16 v[10:13], v[206:209], v[120:123], v[10:13]
	v_mfma_f32_16x16x32_bf16 v[22:25], v[210:213], v[110:113], v[22:25]
	v_mfma_f32_16x16x32_bf16 v[10:13], v[210:213], v[120:123], v[10:13]
	v_mfma_f32_16x16x32_bf16 v[22:25], v[206:209], v[116:119], v[22:25]
	v_mfma_f32_16x16x32_bf16 v[10:13], v[206:209], v[124:127], v[10:13]
	s_and_b64 vcc, exec, s[8:9]
	s_cbranch_vccz .Lrg_skip_5
	v_mfma_f32_16x16x32_bf16 v[18:21], v[214:217], v[110:113], v[18:21]
	v_mfma_f32_16x16x32_bf16 v[6:9], v[214:217], v[120:123], v[6:9]
	v_mfma_f32_16x16x32_bf16 v[18:21], v[218:221], v[110:113], v[18:21]
	v_mfma_f32_16x16x32_bf16 v[6:9], v[218:221], v[120:123], v[6:9]
	v_mfma_f32_16x16x32_bf16 v[18:21], v[214:217], v[116:119], v[18:21]
	v_mfma_f32_16x16x32_bf16 v[6:9], v[214:217], v[124:127], v[6:9]
.Lrg_skip_5:
	global_load_dwordx4 v[198:201], v222, s[98:99] offset:2048
	global_load_dwordx4 v[202:205], v222, s[100:101] offset:2048
	global_load_dwordx4 v[206:209], v223, s[98:99] offset:2048
	global_load_dwordx4 v[210:213], v223, s[100:101] offset:2048
	global_load_dwordx4 v[214:217], v224, s[98:99] offset:2048
	global_load_dwordx4 v[218:221], v224, s[100:101] offset:2048
	v_add_u32_e32 v3, 28, v245
	v_xor_b32_e32 v4, v3, v1
	v_xor_b32_e32 v3, v3, v238
	v_lshl_add_u32 v4, v4, 4, v233
	v_lshl_add_u32 v3, v3, 4, v239
	v_add_u32_e32 v5, s56, v4
	v_add_u32_e32 v115, s56, v3
	ds_read_b128 v[110:113], v4
	ds_read_b128 v[116:119], v5
	ds_read_b128 v[120:123], v3
	ds_read_b128 v[124:127], v115
	s_waitcnt vmcnt(12) lgkmcnt(4)
	v_mfma_f32_16x16x32_bf16 v[26:29], v[150:153], v[34:37], v[26:29]
	v_mfma_f32_16x16x32_bf16 v[14:17], v[150:153], v[42:45], v[14:17]
	v_mfma_f32_16x16x32_bf16 v[26:29], v[154:157], v[34:37], v[26:29]
	v_mfma_f32_16x16x32_bf16 v[14:17], v[154:157], v[42:45], v[14:17]
	v_mfma_f32_16x16x32_bf16 v[26:29], v[150:153], v[30:33], v[26:29]
	v_mfma_f32_16x16x32_bf16 v[14:17], v[150:153], v[38:41], v[14:17]
	v_mfma_f32_16x16x32_bf16 v[22:25], v[158:161], v[34:37], v[22:25]
	v_mfma_f32_16x16x32_bf16 v[10:13], v[158:161], v[42:45], v[10:13]
	v_mfma_f32_16x16x32_bf16 v[22:25], v[162:165], v[34:37], v[22:25]
	v_mfma_f32_16x16x32_bf16 v[10:13], v[162:165], v[42:45], v[10:13]
	v_mfma_f32_16x16x32_bf16 v[22:25], v[158:161], v[30:33], v[22:25]
	v_mfma_f32_16x16x32_bf16 v[10:13], v[158:161], v[38:41], v[10:13]
	s_and_b64 vcc, exec, s[8:9]
	s_cbranch_vccz .Lrg_skip_6
	v_mfma_f32_16x16x32_bf16 v[18:21], v[166:169], v[34:37], v[18:21]
	v_mfma_f32_16x16x32_bf16 v[6:9], v[166:169], v[42:45], v[6:9]
	v_mfma_f32_16x16x32_bf16 v[18:21], v[170:173], v[34:37], v[18:21]
	v_mfma_f32_16x16x32_bf16 v[6:9], v[170:173], v[42:45], v[6:9]
	v_mfma_f32_16x16x32_bf16 v[18:21], v[166:169], v[30:33], v[18:21]
	v_mfma_f32_16x16x32_bf16 v[6:9], v[166:169], v[38:41], v[6:9]
.Lrg_skip_6:
	global_load_dwordx4 v[150:153], v222, s[98:99] offset:2112
	global_load_dwordx4 v[154:157], v222, s[100:101] offset:2112
	global_load_dwordx4 v[158:161], v223, s[98:99] offset:2112
	global_load_dwordx4 v[162:165], v223, s[100:101] offset:2112
	global_load_dwordx4 v[166:169], v224, s[98:99] offset:2112
	global_load_dwordx4 v[170:173], v224, s[100:101] offset:2112
	s_waitcnt vmcnt(12) lgkmcnt(0)
	v_mfma_f32_16x16x32_bf16 v[26:29], v[174:177], v[110:113], v[26:29]
	v_mfma_f32_16x16x32_bf16 v[14:17], v[174:177], v[120:123], v[14:17]
	v_mfma_f32_16x16x32_bf16 v[26:29], v[178:181], v[110:113], v[26:29]
	v_mfma_f32_16x16x32_bf16 v[14:17], v[178:181], v[120:123], v[14:17]
	v_mfma_f32_16x16x32_bf16 v[26:29], v[174:177], v[116:119], v[26:29]
	v_mfma_f32_16x16x32_bf16 v[14:17], v[174:177], v[124:127], v[14:17]
	v_mfma_f32_16x16x32_bf16 v[22:25], v[182:185], v[110:113], v[22:25]
	v_mfma_f32_16x16x32_bf16 v[10:13], v[182:185], v[120:123], v[10:13]
	v_mfma_f32_16x16x32_bf16 v[22:25], v[186:189], v[110:113], v[22:25]
	v_mfma_f32_16x16x32_bf16 v[10:13], v[186:189], v[120:123], v[10:13]
	v_mfma_f32_16x16x32_bf16 v[22:25], v[182:185], v[116:119], v[22:25]
	v_mfma_f32_16x16x32_bf16 v[10:13], v[182:185], v[124:127], v[10:13]
	s_and_b64 vcc, exec, s[8:9]
	s_cbranch_vccz .Lrg_skip_7
	v_mfma_f32_16x16x32_bf16 v[18:21], v[190:193], v[110:113], v[18:21]
	v_mfma_f32_16x16x32_bf16 v[6:9], v[190:193], v[120:123], v[6:9]
	v_mfma_f32_16x16x32_bf16 v[18:21], v[194:197], v[110:113], v[18:21]
	v_mfma_f32_16x16x32_bf16 v[6:9], v[194:197], v[120:123], v[6:9]
	v_mfma_f32_16x16x32_bf16 v[18:21], v[190:193], v[116:119], v[18:21]
	v_mfma_f32_16x16x32_bf16 v[6:9], v[190:193], v[124:127], v[6:9]
.Lrg_skip_7:
.LBB0_897:
	v_mov_b32_e32 v3, v232
	s_waitcnt lgkmcnt(0)
	s_barrier
	s_mov_b64 s[10:11], 0
	v_xor_b32_e32 v3, v3, v129
	v_lshl_add_u32 v3, v3, 4, v240
	v_add_u32_e32 v4, 0, v3
	v_add_u32_e32 v3, s56, v3
	ds_write_b64 v3, v[74:75]
	v_mov_b32_e32 v3, v232
	ds_write_b64 v4, v[70:71]
	s_nop 0
	v_add_u32_e32 v3, 32, v3
	v_xor_b32_e32 v3, v3, v129
	v_lshl_add_u32 v3, v3, 4, v240
	v_add_u32_e32 v4, 0, v3
	v_add_u32_e32 v3, s56, v3
	ds_write_b64 v3, v[82:83]
	v_mov_b32_e32 v3, v232
	ds_write_b64 v4, v[78:79]
	s_nop 0
	v_add_u32_e32 v3, 64, v3
	v_xor_b32_e32 v3, v3, v129
	v_lshl_add_u32 v3, v3, 4, v240
	v_add_u32_e32 v4, 0, v3
	v_add_u32_e32 v3, s56, v3
	ds_write_b64 v3, v[90:91]
	v_mov_b32_e32 v3, v232
	ds_write_b64 v4, v[86:87]
	s_nop 0
	v_add_u32_e32 v3, 0x60, v3
	v_xor_b32_e32 v3, v3, v129
	v_lshl_add_u32 v3, v3, 4, v240
	v_add_u32_e32 v4, 0, v3
	v_add_u32_e32 v3, s56, v3
	ds_write_b64 v3, v[98:99]
	v_mov_b32_e32 v3, v232
	ds_write_b64 v4, v[94:95]
	s_nop 0
	v_xor_b32_e32 v3, v3, v235
	v_lshl_add_u32 v3, v3, 4, v241
	v_add_u32_e32 v4, 0, v3
	v_add_u32_e32 v3, s56, v3
	ds_write_b64 v3, v[76:77]
	v_mov_b32_e32 v3, v232
	ds_write_b64 v4, v[72:73]
	s_nop 0
	v_add_u32_e32 v3, 32, v3
	v_xor_b32_e32 v3, v3, v235
	v_lshl_add_u32 v3, v3, 4, v241
	v_add_u32_e32 v4, 0, v3
	v_add_u32_e32 v3, s56, v3
	ds_write_b64 v3, v[84:85]
	v_mov_b32_e32 v3, v232
	ds_write_b64 v4, v[80:81]
	s_nop 0
	v_add_u32_e32 v3, 64, v3
	v_xor_b32_e32 v3, v3, v235
	v_lshl_add_u32 v3, v3, 4, v241
	v_add_u32_e32 v4, 0, v3
	v_add_u32_e32 v3, s56, v3
	ds_write_b64 v3, v[92:93]
	v_mov_b32_e32 v3, v232
	ds_write_b64 v4, v[88:89]
	s_nop 0
	v_add_u32_e32 v3, 0x60, v3
	v_xor_b32_e32 v3, v3, v235
	v_lshl_add_u32 v3, v3, 4, v241
	v_add_u32_e32 v4, 0, v3
	v_add_u32_e32 v3, s56, v3
	ds_write_b64 v3, v[100:101]
	v_mov_b32_e32 v3, v232
	ds_write_b64 v4, v[96:97]
	s_nop 0
	v_xor_b32_e32 v3, v3, v236
	v_lshl_add_u32 v3, v3, 4, v242
	v_add_u32_e32 v4, 0, v3
	v_add_u32_e32 v3, s56, v3
	ds_write_b64 v3, v[52:53]
	v_mov_b32_e32 v3, v232
	ds_write_b64 v4, v[48:49]
	s_nop 0
	v_add_u32_e32 v3, 32, v3
	v_xor_b32_e32 v3, v3, v236
	v_lshl_add_u32 v3, v3, 4, v242
	v_add_u32_e32 v4, 0, v3
	v_add_u32_e32 v3, s56, v3
	ds_write_b64 v3, v[58:59]
	v_mov_b32_e32 v3, v232
	ds_write_b64 v4, v[46:47]
	s_nop 0
	v_add_u32_e32 v3, 64, v3
	v_xor_b32_e32 v3, v3, v236
	v_lshl_add_u32 v3, v3, 4, v242
	v_add_u32_e32 v4, 0, v3
	v_add_u32_e32 v3, s56, v3
	ds_write_b64 v3, v[66:67]
	v_mov_b32_e32 v3, v232
	ds_write_b64 v4, v[62:63]
	s_nop 0
	v_add_u32_e32 v3, 0x60, v3
	v_xor_b32_e32 v3, v3, v236
	v_lshl_add_u32 v3, v3, 4, v242
	v_add_u32_e32 v4, 0, v3
	v_add_u32_e32 v3, s56, v3
	ds_write_b64 v3, v[106:107]
	v_mov_b32_e32 v3, v232
	ds_write_b64 v4, v[68:69]
	s_nop 0
	v_xor_b32_e32 v3, v3, v237
	v_lshl_add_u32 v3, v3, 4, v243
	v_add_u32_e32 v4, 0, v3
	v_add_u32_e32 v3, s56, v3
	ds_write_b64 v3, v[54:55]
	v_mov_b32_e32 v3, v232
	ds_write_b64 v4, v[50:51]
	s_nop 0
	v_add_u32_e32 v3, 32, v3
	v_xor_b32_e32 v3, v3, v237
	v_lshl_add_u32 v3, v3, 4, v243
	v_add_u32_e32 v4, 0, v3
	v_add_u32_e32 v3, s56, v3
	ds_write_b64 v3, v[60:61]
	v_mov_b32_e32 v3, v232
	ds_write_b64 v4, v[56:57]
	s_nop 0
	v_add_u32_e32 v3, 64, v3
	v_xor_b32_e32 v3, v3, v237
	v_lshl_add_u32 v3, v3, 4, v243
	v_add_u32_e32 v4, 0, v3
	v_add_u32_e32 v3, s56, v3
	ds_write_b64 v3, v[102:103]
	v_mov_b32_e32 v3, v232
	ds_write_b64 v4, v[64:65]
	s_nop 0
	v_add_u32_e32 v3, 0x60, v3
	v_xor_b32_e32 v3, v3, v237
	v_lshl_add_u32 v3, v3, 4, v243
	v_add_u32_e32 v4, 0, v3
	v_add_u32_e32 v3, s56, v3
	ds_write_b64 v3, v[108:109]
	v_mov_b32_e32 v3, v245
	ds_write_b64 v4, v[104:105]
	s_waitcnt lgkmcnt(0)
	s_barrier
	v_mov_b32_e32 v3, v245
	v_xor_b32_e32 v4, v3, v1
	v_xor_b32_e32 v3, v3, v238
	v_lshl_add_u32 v4, v4, 4, v233
	v_lshl_add_u32 v3, v3, 4, v239
	v_add_u32_e32 v5, s56, v4
	v_add_u32_e32 v115, s56, v3
	ds_read_b128 v[34:37], v4
	ds_read_b128 v[30:33], v5
	ds_read_b128 v[42:45], v3
	ds_read_b128 v[38:41], v115
	global_load_dwordx4 v[174:177], v222, s[98:99] offset:2176
	global_load_dwordx4 v[178:181], v222, s[100:101] offset:2176
	global_load_dwordx4 v[182:185], v223, s[98:99] offset:2176
	global_load_dwordx4 v[186:189], v223, s[100:101] offset:2176
	global_load_dwordx4 v[190:193], v224, s[98:99] offset:2176
	global_load_dwordx4 v[194:197], v224, s[100:101] offset:2176
	v_add_u32_e32 v3, 4, v245
	v_xor_b32_e32 v4, v3, v1
	v_xor_b32_e32 v3, v3, v238
	v_lshl_add_u32 v4, v4, 4, v233
	v_lshl_add_u32 v3, v3, 4, v239
	v_add_u32_e32 v5, s56, v4
	v_add_u32_e32 v115, s56, v3
	ds_read_b128 v[110:113], v4
	ds_read_b128 v[116:119], v5
	ds_read_b128 v[120:123], v3
	ds_read_b128 v[124:127], v115
	s_waitcnt vmcnt(12) lgkmcnt(4)
	v_mfma_f32_16x16x32_bf16 v[26:29], v[198:201], v[34:37], v[26:29]
	v_mfma_f32_16x16x32_bf16 v[14:17], v[198:201], v[42:45], v[14:17]
	v_mfma_f32_16x16x32_bf16 v[26:29], v[202:205], v[34:37], v[26:29]
	v_mfma_f32_16x16x32_bf16 v[14:17], v[202:205], v[42:45], v[14:17]
	v_mfma_f32_16x16x32_bf16 v[26:29], v[198:201], v[30:33], v[26:29]
	v_mfma_f32_16x16x32_bf16 v[14:17], v[198:201], v[38:41], v[14:17]
	v_mfma_f32_16x16x32_bf16 v[22:25], v[206:209], v[34:37], v[22:25]
	v_mfma_f32_16x16x32_bf16 v[10:13], v[206:209], v[42:45], v[10:13]
	v_mfma_f32_16x16x32_bf16 v[22:25], v[210:213], v[34:37], v[22:25]
	v_mfma_f32_16x16x32_bf16 v[10:13], v[210:213], v[42:45], v[10:13]
	v_mfma_f32_16x16x32_bf16 v[22:25], v[206:209], v[30:33], v[22:25]
	v_mfma_f32_16x16x32_bf16 v[10:13], v[206:209], v[38:41], v[10:13]
	s_and_b64 vcc, exec, s[8:9]
	s_cbranch_vccz .Lrg_skip_8
	v_mfma_f32_16x16x32_bf16 v[18:21], v[214:217], v[34:37], v[18:21]
	v_mfma_f32_16x16x32_bf16 v[6:9], v[214:217], v[42:45], v[6:9]
	v_mfma_f32_16x16x32_bf16 v[18:21], v[218:221], v[34:37], v[18:21]
	v_mfma_f32_16x16x32_bf16 v[6:9], v[218:221], v[42:45], v[6:9]
	v_mfma_f32_16x16x32_bf16 v[18:21], v[214:217], v[30:33], v[18:21]
	v_mfma_f32_16x16x32_bf16 v[6:9], v[214:217], v[38:41], v[6:9]
.Lrg_skip_8:
	global_load_dwordx4 v[198:201], v222, s[98:99] offset:2240
	global_load_dwordx4 v[202:205], v222, s[100:101] offset:2240
	global_load_dwordx4 v[206:209], v223, s[98:99] offset:2240
	global_load_dwordx4 v[210:213], v223, s[100:101] offset:2240
	global_load_dwordx4 v[214:217], v224, s[98:99] offset:2240
	global_load_dwordx4 v[218:221], v224, s[100:101] offset:2240
	v_add_u32_e32 v3, 8, v245
	v_xor_b32_e32 v4, v3, v1
	v_xor_b32_e32 v3, v3, v238
	v_lshl_add_u32 v4, v4, 4, v233
	v_lshl_add_u32 v3, v3, 4, v239
	v_add_u32_e32 v5, s56, v4
	v_add_u32_e32 v115, s56, v3
	ds_read_b128 v[34:37], v4
	ds_read_b128 v[30:33], v5
	ds_read_b128 v[42:45], v3
	ds_read_b128 v[38:41], v115
	s_waitcnt vmcnt(12) lgkmcnt(4)
	v_mfma_f32_16x16x32_bf16 v[26:29], v[150:153], v[110:113], v[26:29]
	v_mfma_f32_16x16x32_bf16 v[14:17], v[150:153], v[120:123], v[14:17]
	v_mfma_f32_16x16x32_bf16 v[26:29], v[154:157], v[110:113], v[26:29]
	v_mfma_f32_16x16x32_bf16 v[14:17], v[154:157], v[120:123], v[14:17]
	v_mfma_f32_16x16x32_bf16 v[26:29], v[150:153], v[116:119], v[26:29]
	v_mfma_f32_16x16x32_bf16 v[14:17], v[150:153], v[124:127], v[14:17]
	v_mfma_f32_16x16x32_bf16 v[22:25], v[158:161], v[110:113], v[22:25]
	v_mfma_f32_16x16x32_bf16 v[10:13], v[158:161], v[120:123], v[10:13]
	v_mfma_f32_16x16x32_bf16 v[22:25], v[162:165], v[110:113], v[22:25]
	v_mfma_f32_16x16x32_bf16 v[10:13], v[162:165], v[120:123], v[10:13]
	v_mfma_f32_16x16x32_bf16 v[22:25], v[158:161], v[116:119], v[22:25]
	v_mfma_f32_16x16x32_bf16 v[10:13], v[158:161], v[124:127], v[10:13]
	s_and_b64 vcc, exec, s[8:9]
	s_cbranch_vccz .Lrg_skip_9
	v_mfma_f32_16x16x32_bf16 v[18:21], v[166:169], v[110:113], v[18:21]
	v_mfma_f32_16x16x32_bf16 v[6:9], v[166:169], v[120:123], v[6:9]
	v_mfma_f32_16x16x32_bf16 v[18:21], v[170:173], v[110:113], v[18:21]
	v_mfma_f32_16x16x32_bf16 v[6:9], v[170:173], v[120:123], v[6:9]
	v_mfma_f32_16x16x32_bf16 v[18:21], v[166:169], v[116:119], v[18:21]
	v_mfma_f32_16x16x32_bf16 v[6:9], v[166:169], v[124:127], v[6:9]
.Lrg_skip_9:
	global_load_dwordx4 v[150:153], v222, s[98:99] offset:2304
	global_load_dwordx4 v[154:157], v222, s[100:101] offset:2304
	global_load_dwordx4 v[158:161], v223, s[98:99] offset:2304
	global_load_dwordx4 v[162:165], v223, s[100:101] offset:2304
	global_load_dwordx4 v[166:169], v224, s[98:99] offset:2304
	global_load_dwordx4 v[170:173], v224, s[100:101] offset:2304
	v_add_u32_e32 v3, 12, v245
	v_xor_b32_e32 v4, v3, v1
	v_xor_b32_e32 v3, v3, v238
	v_lshl_add_u32 v4, v4, 4, v233
	v_lshl_add_u32 v3, v3, 4, v239
	v_add_u32_e32 v5, s56, v4
	v_add_u32_e32 v115, s56, v3
	ds_read_b128 v[110:113], v4
	ds_read_b128 v[116:119], v5
	ds_read_b128 v[120:123], v3
	ds_read_b128 v[124:127], v115
	s_waitcnt vmcnt(12) lgkmcnt(4)
	v_mfma_f32_16x16x32_bf16 v[26:29], v[174:177], v[34:37], v[26:29]
	v_mfma_f32_16x16x32_bf16 v[14:17], v[174:177], v[42:45], v[14:17]
	v_mfma_f32_16x16x32_bf16 v[26:29], v[178:181], v[34:37], v[26:29]
	v_mfma_f32_16x16x32_bf16 v[14:17], v[178:181], v[42:45], v[14:17]
	v_mfma_f32_16x16x32_bf16 v[26:29], v[174:177], v[30:33], v[26:29]
	v_mfma_f32_16x16x32_bf16 v[14:17], v[174:177], v[38:41], v[14:17]
	v_mfma_f32_16x16x32_bf16 v[22:25], v[182:185], v[34:37], v[22:25]
	v_mfma_f32_16x16x32_bf16 v[10:13], v[182:185], v[42:45], v[10:13]
	v_mfma_f32_16x16x32_bf16 v[22:25], v[186:189], v[34:37], v[22:25]
	v_mfma_f32_16x16x32_bf16 v[10:13], v[186:189], v[42:45], v[10:13]
	v_mfma_f32_16x16x32_bf16 v[22:25], v[182:185], v[30:33], v[22:25]
	v_mfma_f32_16x16x32_bf16 v[10:13], v[182:185], v[38:41], v[10:13]
	s_and_b64 vcc, exec, s[8:9]
	s_cbranch_vccz .Lrg_skip_10
	v_mfma_f32_16x16x32_bf16 v[18:21], v[190:193], v[34:37], v[18:21]
	v_mfma_f32_16x16x32_bf16 v[6:9], v[190:193], v[42:45], v[6:9]
	v_mfma_f32_16x16x32_bf16 v[18:21], v[194:197], v[34:37], v[18:21]
	v_mfma_f32_16x16x32_bf16 v[6:9], v[194:197], v[42:45], v[6:9]
	v_mfma_f32_16x16x32_bf16 v[18:21], v[190:193], v[30:33], v[18:21]
	v_mfma_f32_16x16x32_bf16 v[6:9], v[190:193], v[38:41], v[6:9]
.Lrg_skip_10:
	global_load_dwordx4 v[174:177], v222, s[98:99] offset:2368
	global_load_dwordx4 v[178:181], v222, s[100:101] offset:2368
	global_load_dwordx4 v[182:185], v223, s[98:99] offset:2368
	global_load_dwordx4 v[186:189], v223, s[100:101] offset:2368
	global_load_dwordx4 v[190:193], v224, s[98:99] offset:2368
	global_load_dwordx4 v[194:197], v224, s[100:101] offset:2368
	v_add_u32_e32 v3, 16, v245
	v_xor_b32_e32 v4, v3, v1
	v_xor_b32_e32 v3, v3, v238
	v_lshl_add_u32 v4, v4, 4, v233
	v_lshl_add_u32 v3, v3, 4, v239
	v_add_u32_e32 v5, s56, v4
	v_add_u32_e32 v115, s56, v3
	ds_read_b128 v[34:37], v4
	ds_read_b128 v[30:33], v5
	ds_read_b128 v[42:45], v3
	ds_read_b128 v[38:41], v115
	s_waitcnt vmcnt(12) lgkmcnt(4)
	v_mfma_f32_16x16x32_bf16 v[26:29], v[198:201], v[110:113], v[26:29]
	v_mfma_f32_16x16x32_bf16 v[14:17], v[198:201], v[120:123], v[14:17]
	v_mfma_f32_16x16x32_bf16 v[26:29], v[202:205], v[110:113], v[26:29]
	v_mfma_f32_16x16x32_bf16 v[14:17], v[202:205], v[120:123], v[14:17]
	v_mfma_f32_16x16x32_bf16 v[26:29], v[198:201], v[116:119], v[26:29]
	v_mfma_f32_16x16x32_bf16 v[14:17], v[198:201], v[124:127], v[14:17]
	v_mfma_f32_16x16x32_bf16 v[22:25], v[206:209], v[110:113], v[22:25]
	v_mfma_f32_16x16x32_bf16 v[10:13], v[206:209], v[120:123], v[10:13]
	v_mfma_f32_16x16x32_bf16 v[22:25], v[210:213], v[110:113], v[22:25]
	v_mfma_f32_16x16x32_bf16 v[10:13], v[210:213], v[120:123], v[10:13]
	v_mfma_f32_16x16x32_bf16 v[22:25], v[206:209], v[116:119], v[22:25]
	v_mfma_f32_16x16x32_bf16 v[10:13], v[206:209], v[124:127], v[10:13]
	s_and_b64 vcc, exec, s[8:9]
	s_cbranch_vccz .Lrg_skip_11
	v_mfma_f32_16x16x32_bf16 v[18:21], v[214:217], v[110:113], v[18:21]
	v_mfma_f32_16x16x32_bf16 v[6:9], v[214:217], v[120:123], v[6:9]
	v_mfma_f32_16x16x32_bf16 v[18:21], v[218:221], v[110:113], v[18:21]
	v_mfma_f32_16x16x32_bf16 v[6:9], v[218:221], v[120:123], v[6:9]
	v_mfma_f32_16x16x32_bf16 v[18:21], v[214:217], v[116:119], v[18:21]
	v_mfma_f32_16x16x32_bf16 v[6:9], v[214:217], v[124:127], v[6:9]
.Lrg_skip_11:
	global_load_dwordx4 v[198:201], v222, s[98:99] offset:2432
	global_load_dwordx4 v[202:205], v222, s[100:101] offset:2432
	global_load_dwordx4 v[206:209], v223, s[98:99] offset:2432
	global_load_dwordx4 v[210:213], v223, s[100:101] offset:2432
	global_load_dwordx4 v[214:217], v224, s[98:99] offset:2432
	global_load_dwordx4 v[218:221], v224, s[100:101] offset:2432
	v_add_u32_e32 v3, 20, v245
	v_xor_b32_e32 v4, v3, v1
	v_xor_b32_e32 v3, v3, v238
	v_lshl_add_u32 v4, v4, 4, v233
	v_lshl_add_u32 v3, v3, 4, v239
	v_add_u32_e32 v5, s56, v4
	v_add_u32_e32 v115, s56, v3
	ds_read_b128 v[110:113], v4
	ds_read_b128 v[116:119], v5
	ds_read_b128 v[120:123], v3
	ds_read_b128 v[124:127], v115
	s_waitcnt vmcnt(12) lgkmcnt(4)
	v_mfma_f32_16x16x32_bf16 v[26:29], v[150:153], v[34:37], v[26:29]
	v_mfma_f32_16x16x32_bf16 v[14:17], v[150:153], v[42:45], v[14:17]
	v_mfma_f32_16x16x32_bf16 v[26:29], v[154:157], v[34:37], v[26:29]
	v_mfma_f32_16x16x32_bf16 v[14:17], v[154:157], v[42:45], v[14:17]
	v_mfma_f32_16x16x32_bf16 v[26:29], v[150:153], v[30:33], v[26:29]
	v_mfma_f32_16x16x32_bf16 v[14:17], v[150:153], v[38:41], v[14:17]
	v_mfma_f32_16x16x32_bf16 v[22:25], v[158:161], v[34:37], v[22:25]
	v_mfma_f32_16x16x32_bf16 v[10:13], v[158:161], v[42:45], v[10:13]
	v_mfma_f32_16x16x32_bf16 v[22:25], v[162:165], v[34:37], v[22:25]
	v_mfma_f32_16x16x32_bf16 v[10:13], v[162:165], v[42:45], v[10:13]
	v_mfma_f32_16x16x32_bf16 v[22:25], v[158:161], v[30:33], v[22:25]
	v_mfma_f32_16x16x32_bf16 v[10:13], v[158:161], v[38:41], v[10:13]
	s_and_b64 vcc, exec, s[8:9]
	s_cbranch_vccz .Lrg_skip_12
	v_mfma_f32_16x16x32_bf16 v[18:21], v[166:169], v[34:37], v[18:21]
	v_mfma_f32_16x16x32_bf16 v[6:9], v[166:169], v[42:45], v[6:9]
	v_mfma_f32_16x16x32_bf16 v[18:21], v[170:173], v[34:37], v[18:21]
	v_mfma_f32_16x16x32_bf16 v[6:9], v[170:173], v[42:45], v[6:9]
	v_mfma_f32_16x16x32_bf16 v[18:21], v[166:169], v[30:33], v[18:21]
	v_mfma_f32_16x16x32_bf16 v[6:9], v[166:169], v[38:41], v[6:9]
.Lrg_skip_12:
	global_load_dwordx4 v[150:153], v222, s[98:99] offset:2496
	global_load_dwordx4 v[154:157], v222, s[100:101] offset:2496
	global_load_dwordx4 v[158:161], v223, s[98:99] offset:2496
	global_load_dwordx4 v[162:165], v223, s[100:101] offset:2496
	global_load_dwordx4 v[166:169], v224, s[98:99] offset:2496
	global_load_dwordx4 v[170:173], v224, s[100:101] offset:2496
	v_add_u32_e32 v3, 24, v245
	v_xor_b32_e32 v4, v3, v1
	v_xor_b32_e32 v3, v3, v238
	v_lshl_add_u32 v4, v4, 4, v233
	v_lshl_add_u32 v3, v3, 4, v239
	v_add_u32_e32 v5, s56, v4
	v_add_u32_e32 v115, s56, v3
	ds_read_b128 v[34:37], v4
	ds_read_b128 v[30:33], v5
	ds_read_b128 v[42:45], v3
	ds_read_b128 v[38:41], v115
	s_waitcnt vmcnt(12) lgkmcnt(4)
	v_mfma_f32_16x16x32_bf16 v[26:29], v[174:177], v[110:113], v[26:29]
	v_mfma_f32_16x16x32_bf16 v[14:17], v[174:177], v[120:123], v[14:17]
	v_mfma_f32_16x16x32_bf16 v[26:29], v[178:181], v[110:113], v[26:29]
	v_mfma_f32_16x16x32_bf16 v[14:17], v[178:181], v[120:123], v[14:17]
	v_mfma_f32_16x16x32_bf16 v[26:29], v[174:177], v[116:119], v[26:29]
	v_mfma_f32_16x16x32_bf16 v[14:17], v[174:177], v[124:127], v[14:17]
	v_mfma_f32_16x16x32_bf16 v[22:25], v[182:185], v[110:113], v[22:25]
	v_mfma_f32_16x16x32_bf16 v[10:13], v[182:185], v[120:123], v[10:13]
	v_mfma_f32_16x16x32_bf16 v[22:25], v[186:189], v[110:113], v[22:25]
	v_mfma_f32_16x16x32_bf16 v[10:13], v[186:189], v[120:123], v[10:13]
	v_mfma_f32_16x16x32_bf16 v[22:25], v[182:185], v[116:119], v[22:25]
	v_mfma_f32_16x16x32_bf16 v[10:13], v[182:185], v[124:127], v[10:13]
	s_and_b64 vcc, exec, s[8:9]
	s_cbranch_vccz .Lrg_skip_13
	v_mfma_f32_16x16x32_bf16 v[18:21], v[190:193], v[110:113], v[18:21]
	v_mfma_f32_16x16x32_bf16 v[6:9], v[190:193], v[120:123], v[6:9]
	v_mfma_f32_16x16x32_bf16 v[18:21], v[194:197], v[110:113], v[18:21]
	v_mfma_f32_16x16x32_bf16 v[6:9], v[194:197], v[120:123], v[6:9]
	v_mfma_f32_16x16x32_bf16 v[18:21], v[190:193], v[116:119], v[18:21]
	v_mfma_f32_16x16x32_bf16 v[6:9], v[190:193], v[124:127], v[6:9]
.Lrg_skip_13:
	v_add_u32_e32 v3, 28, v245
	v_xor_b32_e32 v4, v3, v1
	v_xor_b32_e32 v3, v3, v238
	v_lshl_add_u32 v4, v4, 4, v233
	v_lshl_add_u32 v3, v3, 4, v239
	v_add_u32_e32 v5, s56, v4
	v_add_u32_e32 v115, s56, v3
	ds_read_b128 v[110:113], v4
	ds_read_b128 v[116:119], v5
	ds_read_b128 v[120:123], v3
	ds_read_b128 v[124:127], v115
	s_waitcnt vmcnt(6) lgkmcnt(4)
	v_mfma_f32_16x16x32_bf16 v[26:29], v[198:201], v[34:37], v[26:29]
	v_mfma_f32_16x16x32_bf16 v[14:17], v[198:201], v[42:45], v[14:17]
	v_mfma_f32_16x16x32_bf16 v[26:29], v[202:205], v[34:37], v[26:29]
	v_mfma_f32_16x16x32_bf16 v[14:17], v[202:205], v[42:45], v[14:17]
	v_mfma_f32_16x16x32_bf16 v[26:29], v[198:201], v[30:33], v[26:29]
	v_mfma_f32_16x16x32_bf16 v[14:17], v[198:201], v[38:41], v[14:17]
	v_mfma_f32_16x16x32_bf16 v[22:25], v[206:209], v[34:37], v[22:25]
	v_mfma_f32_16x16x32_bf16 v[10:13], v[206:209], v[42:45], v[10:13]
	v_mfma_f32_16x16x32_bf16 v[22:25], v[210:213], v[34:37], v[22:25]
	v_mfma_f32_16x16x32_bf16 v[10:13], v[210:213], v[42:45], v[10:13]
	v_mfma_f32_16x16x32_bf16 v[22:25], v[206:209], v[30:33], v[22:25]
	v_mfma_f32_16x16x32_bf16 v[10:13], v[206:209], v[38:41], v[10:13]
	s_and_b64 vcc, exec, s[8:9]
	s_cbranch_vccz .Lrg_skip_14
	v_mfma_f32_16x16x32_bf16 v[18:21], v[214:217], v[34:37], v[18:21]
	v_mfma_f32_16x16x32_bf16 v[6:9], v[214:217], v[42:45], v[6:9]
	v_mfma_f32_16x16x32_bf16 v[18:21], v[218:221], v[34:37], v[18:21]
	v_mfma_f32_16x16x32_bf16 v[6:9], v[218:221], v[42:45], v[6:9]
	v_mfma_f32_16x16x32_bf16 v[18:21], v[214:217], v[30:33], v[18:21]
	v_mfma_f32_16x16x32_bf16 v[6:9], v[214:217], v[38:41], v[6:9]
.Lrg_skip_14:
	s_waitcnt vmcnt(0) lgkmcnt(0)
	v_mfma_f32_16x16x32_bf16 v[26:29], v[150:153], v[110:113], v[26:29]
	v_mfma_f32_16x16x32_bf16 v[14:17], v[150:153], v[120:123], v[14:17]
	v_mfma_f32_16x16x32_bf16 v[26:29], v[154:157], v[110:113], v[26:29]
	v_mfma_f32_16x16x32_bf16 v[14:17], v[154:157], v[120:123], v[14:17]
	v_mfma_f32_16x16x32_bf16 v[26:29], v[150:153], v[116:119], v[26:29]
	v_mfma_f32_16x16x32_bf16 v[14:17], v[150:153], v[124:127], v[14:17]
	v_mfma_f32_16x16x32_bf16 v[22:25], v[158:161], v[110:113], v[22:25]
	v_mfma_f32_16x16x32_bf16 v[10:13], v[158:161], v[120:123], v[10:13]
	v_mfma_f32_16x16x32_bf16 v[22:25], v[162:165], v[110:113], v[22:25]
	v_mfma_f32_16x16x32_bf16 v[10:13], v[162:165], v[120:123], v[10:13]
	v_mfma_f32_16x16x32_bf16 v[22:25], v[158:161], v[116:119], v[22:25]
	v_mfma_f32_16x16x32_bf16 v[10:13], v[158:161], v[124:127], v[10:13]
	s_and_b64 vcc, exec, s[8:9]
	s_cbranch_vccz .Lrg_skip_15
	v_mfma_f32_16x16x32_bf16 v[18:21], v[166:169], v[110:113], v[18:21]
	v_mfma_f32_16x16x32_bf16 v[6:9], v[166:169], v[120:123], v[6:9]
	v_mfma_f32_16x16x32_bf16 v[18:21], v[170:173], v[110:113], v[18:21]
	v_mfma_f32_16x16x32_bf16 v[6:9], v[170:173], v[120:123], v[6:9]
	v_mfma_f32_16x16x32_bf16 v[18:21], v[166:169], v[116:119], v[18:21]
	v_mfma_f32_16x16x32_bf16 v[6:9], v[166:169], v[124:127], v[6:9]
.Lrg_skip_15:
	s_nop 7
	s_nop 1
